# speedup vs baseline: 1.0066x; 1.0036x over previous
.LBB1_9:
	s_or_b64 exec, exec, s[26:27]
	v_lshlrev_b32_e32 v8, 6, v0
	v_lshlrev_b32_e32 v10, 2, v0
	s_add_i32 s26, 0, 0x20000
	v_and_b32_e32 v84, 48, v0
	v_and_b32_e32 v9, 0x3c0, v8
	v_and_b32_e32 v10, 32, v10
	s_add_u32 s42, s12, s24
	v_bitop3_b32 v85, v9, v10, v84 bitop3:0x36
	s_addc_u32 s43, s13, s25
	v_add_u32_e32 v83, 0, v85
	v_and_b32_e32 v9, 0x4000, v8
	s_add_u32 s44, s14, s0
	v_bfe_u32 v1, v0, 6, 1
	v_lshrrev_b32_e32 v87, 7, v0
	s_waitcnt vmcnt(6)
	v_and_b32_e32 v8, 0x2000, v8
	v_add_u32_e32 v9, v83, v9
	v_add_u32_e32 v82, s23, v85
	v_add_u32_e32 v130, v4, v5
	v_lshlrev_b32_e32 v4, 5, v6
	v_lshlrev_b32_e32 v3, 12, v3
	s_mov_b32 s23, 0x70000
	s_addc_u32 s45, s15, s1
	s_add_i32 s48, 0, 0x18000
	s_add_i32 s49, 0, 0x1c000
	v_lshlrev_b32_e32 v7, 13, v1
	v_add_u32_e32 v10, s26, v85
	v_add_u32_e32 v11, 0x18000, v9
	v_add_u32_e32 v92, v9, v8
	v_and_or_b32 v70, v4, s23, v3
	v_mov_b32_e32 v71, v67
	v_lshl_or_b32 v72, v87, 16, v3
	v_mov_b32_e32 v73, v67
	v_add_u32_e32 v98, s26, v2
	v_add_u32_e32 v147, s48, v2
	v_add_u32_e32 v148, s49, v2
	v_mov_b32_e32 v131, v67
	s_mov_b32 s23, -3
	v_add_u32_e32 v97, v83, v7
	s_mov_b64 s[0:1], 0x1000100
	s_mov_b64 s[24:25], 0x100
	s_mov_b64 s[26:27], 0x80100
	v_add_u32_e32 v96, v82, v7
	s_mov_b64 s[28:29], 0x1000180
	s_mov_b64 s[30:31], 0x180
	s_mov_b64 s[34:35], 0x80180
	v_add_u32_e32 v99, v10, v7
	v_add_u32_e32 v100, v11, v8
	s_mov_b64 s[36:37], 0x1000200
	s_mov_b64 s[38:39], 0x200
	s_mov_b64 s[40:41], 0x80200
	v_mov_b32_e32 v2, v67
	v_mov_b32_e32 v3, v67
	v_mov_b32_e32 v4, v67
	v_mov_b32_e32 v5, v67
	v_mov_b32_e32 v6, v67
	v_mov_b32_e32 v7, v67
	v_mov_b32_e32 v8, v67
	v_mov_b32_e32 v9, v67
	v_mov_b32_e32 v10, v67
	v_mov_b32_e32 v11, v67
	v_mov_b32_e32 v12, v67
	v_mov_b32_e32 v13, v67
	v_mov_b32_e32 v14, v67
	v_mov_b32_e32 v15, v67
	v_mov_b32_e32 v16, v67
	v_mov_b32_e32 v17, v67
	v_mov_b32_e32 v18, v67
	v_mov_b32_e32 v19, v67
	v_mov_b32_e32 v20, v67
	v_mov_b32_e32 v21, v67
	v_mov_b32_e32 v22, v67
	v_mov_b32_e32 v23, v67
	v_mov_b32_e32 v24, v67
	v_mov_b32_e32 v25, v67
	v_mov_b32_e32 v26, v67
	v_mov_b32_e32 v27, v67
	v_mov_b32_e32 v28, v67
	v_mov_b32_e32 v29, v67
	v_mov_b32_e32 v30, v67
	v_mov_b32_e32 v31, v67
	v_mov_b32_e32 v32, v67
	v_mov_b32_e32 v33, v67
	v_mov_b32_e32 v34, v67
	v_mov_b32_e32 v35, v67
	v_mov_b32_e32 v36, v67
	v_mov_b32_e32 v37, v67
	v_mov_b32_e32 v38, v67
	v_mov_b32_e32 v39, v67
	v_mov_b32_e32 v40, v67
	v_mov_b32_e32 v41, v67
	v_mov_b32_e32 v42, v67
	v_mov_b32_e32 v43, v67
	v_mov_b32_e32 v44, v67
	v_mov_b32_e32 v45, v67
	v_mov_b32_e32 v46, v67
	v_mov_b32_e32 v47, v67
	v_mov_b32_e32 v48, v67
	v_mov_b32_e32 v49, v67
	v_mov_b32_e32 v50, v67
	v_mov_b32_e32 v51, v67
	v_mov_b32_e32 v52, v67
	v_mov_b32_e32 v53, v67
	v_mov_b32_e32 v54, v67
	v_mov_b32_e32 v55, v67
	v_mov_b32_e32 v56, v67
	v_mov_b32_e32 v57, v67
	v_mov_b32_e32 v58, v67
	v_mov_b32_e32 v59, v67
	v_mov_b32_e32 v60, v67
	v_mov_b32_e32 v61, v67
	v_mov_b32_e32 v62, v67
	v_mov_b32_e32 v63, v67
	v_mov_b32_e32 v64, v67
	v_mov_b32_e32 v65, v67
	v_add_u32_e32 v101, 0x19000, v92
	v_add_u32_e32 v102, 0x19400, v92
	v_add_u32_e32 v103, 0x19800, v92
	v_add_u32_e32 v104, 0x19c00, v92
	v_add_u32_e32 v105, 0x2000, v98
	v_add_u32_e32 v106, 0x2000, v147
	v_add_u32_e32 v107, 0x2000, v148
	v_add_u32_e32 v108, 0x2000, v145
	v_add_u32_e32 v109, 0x2000, v146
	v_lshl_add_u64 v[74:75], s[42:43], 0, v[70:71]
	v_lshl_add_u64 v[76:77], s[42:43], 0, v[72:73]
	v_lshl_add_u64 v[78:79], s[44:45], 0, v[70:71]
	v_lshl_add_u64 v[80:81], s[44:45], 0, v[72:73]
	s_barrier
	s_barrier
	s_nop 1
	v_readfirstlane_b32 s74, v98
	v_readfirstlane_b32 s75, v105
	v_readfirstlane_b32 s76, v147
	v_readfirstlane_b32 s77, v106
	v_readfirstlane_b32 s78, v148
	v_readfirstlane_b32 s79, v107
	v_readfirstlane_b32 s80, v88
	v_readfirstlane_b32 s81, v89
	v_readfirstlane_b32 s82, v144
	v_readfirstlane_b32 s83, v90
	v_readfirstlane_b32 s84, v91
	v_readfirstlane_b32 s85, v93
	v_readfirstlane_b32 s86, v145
	v_readfirstlane_b32 s87, v108
	v_readfirstlane_b32 s88, v94
	v_readfirstlane_b32 s89, v95
	v_readfirstlane_b32 s90, v146
	v_readfirstlane_b32 s91, v109
	v_lshl_add_u64 v[182:183], v[80:81], 0, v[130:131]
	v_lshl_add_u64 v[110:111], v[182:183], 0, s[0:1]
	s_mov_b32 m0, s74
	v_lshl_add_u64 v[184:185], v[78:79], 0, v[130:131]
	global_load_lds_dwordx4 v[110:111], off
	v_lshl_add_u64 v[110:111], v[184:185], 0, s[0:1]
	s_mov_b32 m0, s75
	v_lshl_add_u64 v[186:187], v[76:77], 0, v[130:131]
	global_load_lds_dwordx4 v[110:111], off
	v_lshl_add_u64 v[110:111], v[186:187], 0, s[24:25]
	s_mov_b32 m0, s76
	v_lshl_add_u64 v[188:189], v[74:75], 0, v[130:131]
	global_load_lds_dwordx4 v[110:111], off
	v_lshl_add_u64 v[110:111], v[188:189], 0, s[24:25]
	s_mov_b32 m0, s77
	s_nop 0
	global_load_lds_dwordx4 v[110:111], off
	v_lshl_add_u64 v[110:111], v[186:187], 0, s[26:27]
	s_mov_b32 m0, s78
	s_nop 0
	global_load_lds_dwordx4 v[110:111], off
	v_lshl_add_u64 v[110:111], v[188:189], 0, s[26:27]
	s_mov_b32 m0, s79
	s_nop 0
	global_load_lds_dwordx4 v[110:111], off
	ds_read_b128 v[110:113], v97 offset:32768
	ds_read_b128 v[114:117], v97 offset:33792
	ds_read_b128 v[118:121], v97 offset:34816
	ds_read_b128 v[122:125], v97 offset:35840
	ds_read_b128 v[126:129], v97 offset:36864
	ds_read_b128 v[132:135], v97 offset:37888
	ds_read_b128 v[136:139], v97 offset:38912
	ds_read_b128 v[140:143], v97 offset:39936
	ds_read_b128 v[150:153], v92
	ds_read_b128 v[154:157], v92 offset:1024
	ds_read_b128 v[158:161], v92 offset:2048
	ds_read_b128 v[162:165], v92 offset:3072
	ds_read_b128 v[166:169], v92 offset:4096
	ds_read_b128 v[170:173], v92 offset:5120
	ds_read_b128 v[174:177], v92 offset:6144
	ds_read_b128 v[178:181], v92 offset:7168
	s_waitcnt vmcnt(6)
	s_waitcnt lgkmcnt(0)
	s_barrier
	s_setprio 1
	s_waitcnt lgkmcnt(0)
	v_mfma_f32_16x16x32_f16 v[62:65], v[110:113], v[150:153], v[62:65]
	s_lshl_b32 s60, s66, 16
	s_add_u32 s62, s58, s60
	s_addc_u32 s63, s59, 0
	s_lshl_b32 s61, s66, 15
	s_add_u32 s64, s52, s61
	s_addc_u32 s65, s53, 0
	v_lshlrev_b32_e32 v254, 5, v0
	v_lshlrev_b32_e32 v255, 4, v0
	global_load_dwordx4 v[230:233], v254, s[62:63] nt
	v_mfma_f32_16x16x32_f16 v[58:61], v[118:121], v[150:153], v[58:61]
	global_load_dwordx4 v[234:237], v254, s[62:63] offset:16 nt
	v_mfma_f32_16x16x32_f16 v[54:57], v[126:129], v[150:153], v[54:57]
	s_add_u32 s62, s62, 0x4000
	s_addc_u32 s63, s63, 0
	global_load_dwordx4 v[238:241], v254, s[62:63] nt
	v_mfma_f32_16x16x32_f16 v[50:53], v[136:139], v[150:153], v[50:53]
	global_load_dwordx4 v[242:245], v254, s[62:63] offset:16 nt
	v_mfma_f32_16x16x32_f16 v[46:49], v[110:113], v[158:161], v[46:49]
	s_add_u32 s62, s62, 0x4000
	s_addc_u32 s63, s63, 0
	global_load_dwordx4 v[246:249], v254, s[62:63] nt
	v_mfma_f32_16x16x32_f16 v[42:45], v[118:121], v[158:161], v[42:45]
	global_load_dwordx4 v[250:253], v254, s[62:63] offset:16 nt
	v_mfma_f32_16x16x32_f16 v[38:41], v[126:129], v[158:161], v[38:41]
	s_add_u32 s62, s62, 0x4000
	s_addc_u32 s63, s63, 0
	global_load_dwordx4 v[190:193], v254, s[62:63] nt
	v_mfma_f32_16x16x32_f16 v[34:37], v[136:139], v[158:161], v[34:37]
	global_load_dwordx4 v[194:197], v254, s[62:63] offset:16 nt
	v_mfma_f32_16x16x32_f16 v[30:33], v[110:113], v[166:169], v[30:33]
	v_mfma_f32_16x16x32_f16 v[26:29], v[118:121], v[166:169], v[26:29]
	v_mfma_f32_16x16x32_f16 v[22:25], v[126:129], v[166:169], v[22:25]
	v_mfma_f32_16x16x32_f16 v[18:21], v[136:139], v[166:169], v[18:21]
	v_mfma_f32_16x16x32_f16 v[14:17], v[110:113], v[174:177], v[14:17]
	v_mfma_f32_16x16x32_f16 v[10:13], v[118:121], v[174:177], v[10:13]
	v_mfma_f32_16x16x32_f16 v[6:9], v[126:129], v[174:177], v[6:9]
	v_mfma_f32_16x16x32_f16 v[2:5], v[136:139], v[174:177], v[2:5]
	v_mfma_f32_16x16x32_f16 v[62:65], v[114:117], v[154:157], v[62:65]
	v_mfma_f32_16x16x32_f16 v[58:61], v[122:125], v[154:157], v[58:61]
	v_mfma_f32_16x16x32_f16 v[54:57], v[132:135], v[154:157], v[54:57]
	v_mfma_f32_16x16x32_f16 v[50:53], v[140:143], v[154:157], v[50:53]
	v_mfma_f32_16x16x32_f16 v[46:49], v[114:117], v[162:165], v[46:49]
	v_mfma_f32_16x16x32_f16 v[42:45], v[122:125], v[162:165], v[42:45]
	v_mfma_f32_16x16x32_f16 v[38:41], v[132:135], v[162:165], v[38:41]
	v_mfma_f32_16x16x32_f16 v[34:37], v[140:143], v[162:165], v[34:37]
	v_mfma_f32_16x16x32_f16 v[30:33], v[114:117], v[170:173], v[30:33]
	v_mfma_f32_16x16x32_f16 v[26:29], v[122:125], v[170:173], v[26:29]
	v_mfma_f32_16x16x32_f16 v[22:25], v[132:135], v[170:173], v[22:25]
	v_mfma_f32_16x16x32_f16 v[18:21], v[140:143], v[170:173], v[18:21]
	v_mfma_f32_16x16x32_f16 v[14:17], v[114:117], v[178:181], v[14:17]
	v_mfma_f32_16x16x32_f16 v[10:13], v[122:125], v[178:181], v[10:13]
	v_mfma_f32_16x16x32_f16 v[6:9], v[132:135], v[178:181], v[6:9]
	v_mfma_f32_16x16x32_f16 v[2:5], v[140:143], v[178:181], v[2:5]
	s_setprio 0
	s_barrier
	v_lshl_add_u64 v[150:151], v[182:183], 0, s[28:29]
	s_mov_b32 m0, s80
	ds_read_b128 v[110:113], v92 offset:49152
	ds_read_b128 v[114:117], v92 offset:50176
	ds_read_b128 v[118:121], v92 offset:51200
	ds_read_b128 v[122:125], v92 offset:52224
	ds_read_b128 v[126:129], v92 offset:53248
	ds_read_b128 v[132:135], v92 offset:54272
	ds_read_b128 v[136:139], v92 offset:55296
	ds_read_b128 v[140:143], v92 offset:56320
	global_load_lds_dwordx4 v[150:151], off
	v_lshl_add_u64 v[150:151], v[184:185], 0, s[28:29]
	s_mov_b32 m0, s81
	s_nop 0
	global_load_lds_dwordx4 v[150:151], off
	v_lshl_add_u64 v[150:151], v[186:187], 0, s[30:31]
	s_mov_b32 m0, s82
	s_nop 0
	global_load_lds_dwordx4 v[150:151], off
	v_lshl_add_u64 v[150:151], v[188:189], 0, s[30:31]
	s_mov_b32 m0, s83
	s_nop 0
	global_load_lds_dwordx4 v[150:151], off
	v_lshl_add_u64 v[150:151], v[186:187], 0, s[34:35]
	s_mov_b32 m0, s84
	s_nop 0
	global_load_lds_dwordx4 v[150:151], off
	v_lshl_add_u64 v[150:151], v[188:189], 0, s[34:35]
	s_mov_b32 m0, s85
	s_nop 0
	global_load_lds_dwordx4 v[150:151], off
	ds_read_b128 v[150:153], v96
	ds_read_b128 v[154:157], v96 offset:1024
	ds_read_b128 v[158:161], v96 offset:2048
	ds_read_b128 v[162:165], v96 offset:3072
	ds_read_b128 v[166:169], v96 offset:4096
	ds_read_b128 v[170:173], v96 offset:5120
	ds_read_b128 v[174:177], v96 offset:6144
	ds_read_b128 v[178:181], v96 offset:7168
	s_waitcnt vmcnt(14)
	s_waitcnt lgkmcnt(0)
	s_barrier
	s_setprio 1
	s_waitcnt lgkmcnt(0)
	v_mfma_f32_16x16x32_f16 v[62:65], v[150:153], v[110:113], v[62:65]
	v_mfma_f32_16x16x32_f16 v[58:61], v[158:161], v[110:113], v[58:61]
	v_mfma_f32_16x16x32_f16 v[54:57], v[166:169], v[110:113], v[54:57]
	v_mfma_f32_16x16x32_f16 v[50:53], v[174:177], v[110:113], v[50:53]
	v_mfma_f32_16x16x32_f16 v[46:49], v[150:153], v[118:121], v[46:49]
	v_mfma_f32_16x16x32_f16 v[42:45], v[158:161], v[118:121], v[42:45]
	v_mfma_f32_16x16x32_f16 v[38:41], v[166:169], v[118:121], v[38:41]
	v_mfma_f32_16x16x32_f16 v[34:37], v[174:177], v[118:121], v[34:37]
	v_mfma_f32_16x16x32_f16 v[30:33], v[150:153], v[126:129], v[30:33]
	v_mfma_f32_16x16x32_f16 v[26:29], v[158:161], v[126:129], v[26:29]
	v_mfma_f32_16x16x32_f16 v[22:25], v[166:169], v[126:129], v[22:25]
	v_mfma_f32_16x16x32_f16 v[18:21], v[174:177], v[126:129], v[18:21]
	v_mfma_f32_16x16x32_f16 v[14:17], v[150:153], v[136:139], v[14:17]
	v_mfma_f32_16x16x32_f16 v[10:13], v[158:161], v[136:139], v[10:13]
	v_mfma_f32_16x16x32_f16 v[6:9], v[166:169], v[136:139], v[6:9]
	v_mfma_f32_16x16x32_f16 v[2:5], v[174:177], v[136:139], v[2:5]
	v_mfma_f32_16x16x32_f16 v[62:65], v[154:157], v[114:117], v[62:65]
	v_mfma_f32_16x16x32_f16 v[58:61], v[162:165], v[114:117], v[58:61]
	v_mfma_f32_16x16x32_f16 v[54:57], v[170:173], v[114:117], v[54:57]
	v_mfma_f32_16x16x32_f16 v[50:53], v[178:181], v[114:117], v[50:53]
	v_mfma_f32_16x16x32_f16 v[46:49], v[154:157], v[122:125], v[46:49]
	v_mfma_f32_16x16x32_f16 v[42:45], v[162:165], v[122:125], v[42:45]
	v_mfma_f32_16x16x32_f16 v[38:41], v[170:173], v[122:125], v[38:41]
	v_mfma_f32_16x16x32_f16 v[34:37], v[178:181], v[122:125], v[34:37]
	v_mfma_f32_16x16x32_f16 v[30:33], v[154:157], v[132:135], v[30:33]
	v_mfma_f32_16x16x32_f16 v[26:29], v[162:165], v[132:135], v[26:29]
	v_mfma_f32_16x16x32_f16 v[22:25], v[170:173], v[132:135], v[22:25]
	v_mfma_f32_16x16x32_f16 v[18:21], v[178:181], v[132:135], v[18:21]
	v_mfma_f32_16x16x32_f16 v[14:17], v[154:157], v[140:143], v[14:17]
	v_mfma_f32_16x16x32_f16 v[10:13], v[162:165], v[140:143], v[10:13]
	v_mfma_f32_16x16x32_f16 v[6:9], v[170:173], v[140:143], v[6:9]
	v_mfma_f32_16x16x32_f16 v[2:5], v[178:181], v[140:143], v[2:5]
	s_setprio 0
	s_barrier
	v_lshl_add_u64 v[150:151], v[182:183], 0, s[36:37]
	s_mov_b32 m0, s86
	ds_read_b128 v[110:113], v100
	ds_read_b128 v[114:117], v100 offset:1024
	ds_read_b128 v[118:121], v100 offset:2048
	ds_read_b128 v[122:125], v100 offset:3072
	ds_read_b128 v[126:129], v101
	ds_read_b128 v[132:135], v102
	ds_read_b128 v[136:139], v103
	ds_read_b128 v[140:143], v104
	global_load_lds_dwordx4 v[150:151], off
	v_lshl_add_u64 v[150:151], v[184:185], 0, s[36:37]
	s_mov_b32 m0, s87
	s_nop 0
	global_load_lds_dwordx4 v[150:151], off
	v_lshl_add_u64 v[150:151], v[186:187], 0, s[38:39]
	s_mov_b32 m0, s88
	s_nop 0
	global_load_lds_dwordx4 v[150:151], off
	v_lshl_add_u64 v[150:151], v[188:189], 0, s[38:39]
	s_mov_b32 m0, s89
	s_nop 0
	global_load_lds_dwordx4 v[150:151], off
	v_lshl_add_u64 v[150:151], v[186:187], 0, s[40:41]
	s_mov_b32 m0, s90
	s_nop 0
	global_load_lds_dwordx4 v[150:151], off
	v_lshl_add_u64 v[150:151], v[188:189], 0, s[40:41]
	s_mov_b32 m0, s91
	s_nop 0
	global_load_lds_dwordx4 v[150:151], off
	ds_read_b128 v[150:153], v99
	ds_read_b128 v[154:157], v99 offset:1024
	ds_read_b128 v[158:161], v99 offset:2048
	ds_read_b128 v[162:165], v99 offset:3072
	ds_read_b128 v[166:169], v99 offset:4096
	ds_read_b128 v[170:173], v99 offset:5120
	ds_read_b128 v[174:177], v99 offset:6144
	ds_read_b128 v[178:181], v99 offset:7168
	s_waitcnt vmcnt(6)
	s_waitcnt lgkmcnt(0)
	s_barrier
	s_setprio 1
	s_waitcnt lgkmcnt(0)
	v_mfma_f32_16x16x32_f16 v[62:65], v[150:153], v[110:113], v[62:65]
	v_cvt_pk_f16_f32 v230, v230, v231
	v_mfma_f32_16x16x32_f16 v[58:61], v[158:161], v[110:113], v[58:61]
	v_cvt_pk_f16_f32 v231, v232, v233
	v_mfma_f32_16x16x32_f16 v[54:57], v[166:169], v[110:113], v[54:57]
	v_cvt_pk_f16_f32 v232, v234, v235
	v_mfma_f32_16x16x32_f16 v[50:53], v[174:177], v[110:113], v[50:53]
	v_cvt_pk_f16_f32 v233, v236, v237
	v_mfma_f32_16x16x32_f16 v[46:49], v[150:153], v[118:121], v[46:49]
	global_store_dwordx4 v255, v[230:233], s[64:65]
	v_mfma_f32_16x16x32_f16 v[42:45], v[158:161], v[118:121], v[42:45]
	s_add_u32 s64, s64, 0x2000
	s_addc_u32 s65, s65, 0
	v_mfma_f32_16x16x32_f16 v[38:41], v[166:169], v[118:121], v[38:41]
	v_cvt_pk_f16_f32 v238, v238, v239
	v_mfma_f32_16x16x32_f16 v[34:37], v[174:177], v[118:121], v[34:37]
	v_cvt_pk_f16_f32 v239, v240, v241
	v_mfma_f32_16x16x32_f16 v[30:33], v[150:153], v[126:129], v[30:33]
	v_cvt_pk_f16_f32 v240, v242, v243
	v_mfma_f32_16x16x32_f16 v[26:29], v[158:161], v[126:129], v[26:29]
	v_cvt_pk_f16_f32 v241, v244, v245
	v_mfma_f32_16x16x32_f16 v[22:25], v[166:169], v[126:129], v[22:25]
	global_store_dwordx4 v255, v[238:241], s[64:65]
	v_mfma_f32_16x16x32_f16 v[18:21], v[174:177], v[126:129], v[18:21]
	s_add_u32 s64, s64, 0x2000
	s_addc_u32 s65, s65, 0
	v_mfma_f32_16x16x32_f16 v[14:17], v[150:153], v[136:139], v[14:17]
	v_cvt_pk_f16_f32 v246, v246, v247
	v_mfma_f32_16x16x32_f16 v[10:13], v[158:161], v[136:139], v[10:13]
	v_cvt_pk_f16_f32 v247, v248, v249
	v_mfma_f32_16x16x32_f16 v[6:9], v[166:169], v[136:139], v[6:9]
	v_cvt_pk_f16_f32 v248, v250, v251
	v_mfma_f32_16x16x32_f16 v[2:5], v[174:177], v[136:139], v[2:5]
	v_cvt_pk_f16_f32 v249, v252, v253
	v_mfma_f32_16x16x32_f16 v[62:65], v[154:157], v[114:117], v[62:65]
	global_store_dwordx4 v255, v[246:249], s[64:65]
	v_mfma_f32_16x16x32_f16 v[58:61], v[162:165], v[114:117], v[58:61]
	s_add_u32 s64, s64, 0x2000
	s_addc_u32 s65, s65, 0
	v_mfma_f32_16x16x32_f16 v[54:57], v[170:173], v[114:117], v[54:57]
	v_cvt_pk_f16_f32 v190, v190, v191
	v_mfma_f32_16x16x32_f16 v[50:53], v[178:181], v[114:117], v[50:53]
	v_cvt_pk_f16_f32 v191, v192, v193
	v_mfma_f32_16x16x32_f16 v[46:49], v[154:157], v[122:125], v[46:49]
	v_cvt_pk_f16_f32 v192, v194, v195
	v_mfma_f32_16x16x32_f16 v[42:45], v[162:165], v[122:125], v[42:45]
	v_cvt_pk_f16_f32 v193, v196, v197
	v_mfma_f32_16x16x32_f16 v[38:41], v[170:173], v[122:125], v[38:41]
	global_store_dwordx4 v255, v[190:193], s[64:65]
	v_mfma_f32_16x16x32_f16 v[34:37], v[178:181], v[122:125], v[34:37]
	v_mfma_f32_16x16x32_f16 v[30:33], v[154:157], v[132:135], v[30:33]
	v_mfma_f32_16x16x32_f16 v[26:29], v[162:165], v[132:135], v[26:29]
	v_mfma_f32_16x16x32_f16 v[22:25], v[170:173], v[132:135], v[22:25]
	v_mfma_f32_16x16x32_f16 v[18:21], v[178:181], v[132:135], v[18:21]
	v_mfma_f32_16x16x32_f16 v[14:17], v[154:157], v[140:143], v[14:17]
	v_mfma_f32_16x16x32_f16 v[10:13], v[162:165], v[140:143], v[10:13]
	v_mfma_f32_16x16x32_f16 v[6:9], v[170:173], v[140:143], v[6:9]
	v_mfma_f32_16x16x32_f16 v[2:5], v[178:181], v[140:143], v[2:5]
	s_setprio 0
	s_barrier
	s_add_i32 s23, s23, 3
	v_lshl_add_u64 v[74:75], v[74:75], 0, s[30:31]
	v_lshl_add_u64 v[76:77], v[76:77], 0, s[30:31]
	v_lshl_add_u64 v[78:79], v[78:79], 0, s[30:31]
	v_lshl_add_u64 v[80:81], v[80:81], 0, s[30:31]
.LBB1_10:
	v_lshl_add_u64 v[182:183], v[80:81], 0, v[130:131]
	v_lshl_add_u64 v[110:111], v[182:183], 0, s[0:1]
	s_mov_b32 m0, s74
	v_lshl_add_u64 v[184:185], v[78:79], 0, v[130:131]
	global_load_lds_dwordx4 v[110:111], off
	v_lshl_add_u64 v[110:111], v[184:185], 0, s[0:1]
	s_mov_b32 m0, s75
	v_lshl_add_u64 v[186:187], v[76:77], 0, v[130:131]
	global_load_lds_dwordx4 v[110:111], off
	v_lshl_add_u64 v[110:111], v[186:187], 0, s[24:25]
	s_mov_b32 m0, s76
	v_lshl_add_u64 v[188:189], v[74:75], 0, v[130:131]
	global_load_lds_dwordx4 v[110:111], off
	v_lshl_add_u64 v[110:111], v[188:189], 0, s[24:25]
	s_mov_b32 m0, s77
	s_nop 0
	global_load_lds_dwordx4 v[110:111], off
	v_lshl_add_u64 v[110:111], v[186:187], 0, s[26:27]
	s_mov_b32 m0, s78
	s_nop 0
	global_load_lds_dwordx4 v[110:111], off
	v_lshl_add_u64 v[110:111], v[188:189], 0, s[26:27]
	s_mov_b32 m0, s79
	s_nop 0
	global_load_lds_dwordx4 v[110:111], off
	ds_read_b128 v[110:113], v97 offset:32768
	ds_read_b128 v[114:117], v97 offset:33792
	ds_read_b128 v[118:121], v97 offset:34816
	ds_read_b128 v[122:125], v97 offset:35840
	ds_read_b128 v[126:129], v97 offset:36864
	ds_read_b128 v[132:135], v97 offset:37888
	ds_read_b128 v[136:139], v97 offset:38912
	ds_read_b128 v[140:143], v97 offset:39936
	ds_read_b128 v[150:153], v92
	ds_read_b128 v[154:157], v92 offset:1024
	ds_read_b128 v[158:161], v92 offset:2048
	ds_read_b128 v[162:165], v92 offset:3072
	ds_read_b128 v[166:169], v92 offset:4096
	ds_read_b128 v[170:173], v92 offset:5120
	ds_read_b128 v[174:177], v92 offset:6144
	ds_read_b128 v[178:181], v92 offset:7168
	s_waitcnt vmcnt(6)
	s_waitcnt lgkmcnt(0)
	s_barrier
	s_setprio 1
	s_waitcnt lgkmcnt(0)
	v_mfma_f32_16x16x32_f16 v[62:65], v[110:113], v[150:153], v[62:65]
	v_mfma_f32_16x16x32_f16 v[58:61], v[118:121], v[150:153], v[58:61]
	v_mfma_f32_16x16x32_f16 v[54:57], v[126:129], v[150:153], v[54:57]
	v_mfma_f32_16x16x32_f16 v[50:53], v[136:139], v[150:153], v[50:53]
	v_mfma_f32_16x16x32_f16 v[46:49], v[110:113], v[158:161], v[46:49]
	v_mfma_f32_16x16x32_f16 v[42:45], v[118:121], v[158:161], v[42:45]
	v_mfma_f32_16x16x32_f16 v[38:41], v[126:129], v[158:161], v[38:41]
	v_mfma_f32_16x16x32_f16 v[34:37], v[136:139], v[158:161], v[34:37]
	v_mfma_f32_16x16x32_f16 v[30:33], v[110:113], v[166:169], v[30:33]
	v_mfma_f32_16x16x32_f16 v[26:29], v[118:121], v[166:169], v[26:29]
	v_mfma_f32_16x16x32_f16 v[22:25], v[126:129], v[166:169], v[22:25]
	v_mfma_f32_16x16x32_f16 v[18:21], v[136:139], v[166:169], v[18:21]
	v_mfma_f32_16x16x32_f16 v[14:17], v[110:113], v[174:177], v[14:17]
	v_mfma_f32_16x16x32_f16 v[10:13], v[118:121], v[174:177], v[10:13]
	v_mfma_f32_16x16x32_f16 v[6:9], v[126:129], v[174:177], v[6:9]
	v_mfma_f32_16x16x32_f16 v[2:5], v[136:139], v[174:177], v[2:5]
	v_mfma_f32_16x16x32_f16 v[62:65], v[114:117], v[154:157], v[62:65]
	v_mfma_f32_16x16x32_f16 v[58:61], v[122:125], v[154:157], v[58:61]
	v_mfma_f32_16x16x32_f16 v[54:57], v[132:135], v[154:157], v[54:57]
	v_mfma_f32_16x16x32_f16 v[50:53], v[140:143], v[154:157], v[50:53]
	v_mfma_f32_16x16x32_f16 v[46:49], v[114:117], v[162:165], v[46:49]
	v_mfma_f32_16x16x32_f16 v[42:45], v[122:125], v[162:165], v[42:45]
	v_mfma_f32_16x16x32_f16 v[38:41], v[132:135], v[162:165], v[38:41]
	v_mfma_f32_16x16x32_f16 v[34:37], v[140:143], v[162:165], v[34:37]
	v_mfma_f32_16x16x32_f16 v[30:33], v[114:117], v[170:173], v[30:33]
	v_mfma_f32_16x16x32_f16 v[26:29], v[122:125], v[170:173], v[26:29]
	v_mfma_f32_16x16x32_f16 v[22:25], v[132:135], v[170:173], v[22:25]
	v_mfma_f32_16x16x32_f16 v[18:21], v[140:143], v[170:173], v[18:21]
	v_mfma_f32_16x16x32_f16 v[14:17], v[114:117], v[178:181], v[14:17]
	v_mfma_f32_16x16x32_f16 v[10:13], v[122:125], v[178:181], v[10:13]
	v_mfma_f32_16x16x32_f16 v[6:9], v[132:135], v[178:181], v[6:9]
	v_mfma_f32_16x16x32_f16 v[2:5], v[140:143], v[178:181], v[2:5]
	s_setprio 0
	s_barrier
	v_lshl_add_u64 v[150:151], v[182:183], 0, s[28:29]
	s_mov_b32 m0, s80
	ds_read_b128 v[110:113], v92 offset:49152
	ds_read_b128 v[114:117], v92 offset:50176
	ds_read_b128 v[118:121], v92 offset:51200
	ds_read_b128 v[122:125], v92 offset:52224
	ds_read_b128 v[126:129], v92 offset:53248
	ds_read_b128 v[132:135], v92 offset:54272
	ds_read_b128 v[136:139], v92 offset:55296
	ds_read_b128 v[140:143], v92 offset:56320
	global_load_lds_dwordx4 v[150:151], off
	v_lshl_add_u64 v[150:151], v[184:185], 0, s[28:29]
	s_mov_b32 m0, s81
	s_nop 0
	global_load_lds_dwordx4 v[150:151], off
	v_lshl_add_u64 v[150:151], v[186:187], 0, s[30:31]
	s_mov_b32 m0, s82
	s_nop 0
	global_load_lds_dwordx4 v[150:151], off
	v_lshl_add_u64 v[150:151], v[188:189], 0, s[30:31]
	s_mov_b32 m0, s83
	s_nop 0
	global_load_lds_dwordx4 v[150:151], off
	v_lshl_add_u64 v[150:151], v[186:187], 0, s[34:35]
	s_mov_b32 m0, s84
	s_nop 0
	global_load_lds_dwordx4 v[150:151], off
	v_lshl_add_u64 v[150:151], v[188:189], 0, s[34:35]
	s_mov_b32 m0, s85
	s_nop 0
	global_load_lds_dwordx4 v[150:151], off
	ds_read_b128 v[150:153], v96
	ds_read_b128 v[154:157], v96 offset:1024
	ds_read_b128 v[158:161], v96 offset:2048
	ds_read_b128 v[162:165], v96 offset:3072
	ds_read_b128 v[166:169], v96 offset:4096
	ds_read_b128 v[170:173], v96 offset:5120
	ds_read_b128 v[174:177], v96 offset:6144
	ds_read_b128 v[178:181], v96 offset:7168
	s_waitcnt vmcnt(6)
	s_waitcnt lgkmcnt(0)
	s_barrier
	s_setprio 1
	s_waitcnt lgkmcnt(0)
	v_mfma_f32_16x16x32_f16 v[62:65], v[150:153], v[110:113], v[62:65]
	v_mfma_f32_16x16x32_f16 v[58:61], v[158:161], v[110:113], v[58:61]
	v_mfma_f32_16x16x32_f16 v[54:57], v[166:169], v[110:113], v[54:57]
	v_mfma_f32_16x16x32_f16 v[50:53], v[174:177], v[110:113], v[50:53]
	v_mfma_f32_16x16x32_f16 v[46:49], v[150:153], v[118:121], v[46:49]
	v_mfma_f32_16x16x32_f16 v[42:45], v[158:161], v[118:121], v[42:45]
	v_mfma_f32_16x16x32_f16 v[38:41], v[166:169], v[118:121], v[38:41]
	v_mfma_f32_16x16x32_f16 v[34:37], v[174:177], v[118:121], v[34:37]
	v_mfma_f32_16x16x32_f16 v[30:33], v[150:153], v[126:129], v[30:33]
	v_mfma_f32_16x16x32_f16 v[26:29], v[158:161], v[126:129], v[26:29]
	v_mfma_f32_16x16x32_f16 v[22:25], v[166:169], v[126:129], v[22:25]
	v_mfma_f32_16x16x32_f16 v[18:21], v[174:177], v[126:129], v[18:21]
	v_mfma_f32_16x16x32_f16 v[14:17], v[150:153], v[136:139], v[14:17]
	v_mfma_f32_16x16x32_f16 v[10:13], v[158:161], v[136:139], v[10:13]
	v_mfma_f32_16x16x32_f16 v[6:9], v[166:169], v[136:139], v[6:9]
	v_mfma_f32_16x16x32_f16 v[2:5], v[174:177], v[136:139], v[2:5]
	v_mfma_f32_16x16x32_f16 v[62:65], v[154:157], v[114:117], v[62:65]
	v_mfma_f32_16x16x32_f16 v[58:61], v[162:165], v[114:117], v[58:61]
	v_mfma_f32_16x16x32_f16 v[54:57], v[170:173], v[114:117], v[54:57]
	v_mfma_f32_16x16x32_f16 v[50:53], v[178:181], v[114:117], v[50:53]
	v_mfma_f32_16x16x32_f16 v[46:49], v[154:157], v[122:125], v[46:49]
	v_mfma_f32_16x16x32_f16 v[42:45], v[162:165], v[122:125], v[42:45]
	v_mfma_f32_16x16x32_f16 v[38:41], v[170:173], v[122:125], v[38:41]
	v_mfma_f32_16x16x32_f16 v[34:37], v[178:181], v[122:125], v[34:37]
	v_mfma_f32_16x16x32_f16 v[30:33], v[154:157], v[132:135], v[30:33]
	v_mfma_f32_16x16x32_f16 v[26:29], v[162:165], v[132:135], v[26:29]
	v_mfma_f32_16x16x32_f16 v[22:25], v[170:173], v[132:135], v[22:25]
	v_mfma_f32_16x16x32_f16 v[18:21], v[178:181], v[132:135], v[18:21]
	v_mfma_f32_16x16x32_f16 v[14:17], v[154:157], v[140:143], v[14:17]
	v_mfma_f32_16x16x32_f16 v[10:13], v[162:165], v[140:143], v[10:13]
	v_mfma_f32_16x16x32_f16 v[6:9], v[170:173], v[140:143], v[6:9]
	v_mfma_f32_16x16x32_f16 v[2:5], v[178:181], v[140:143], v[2:5]
	s_setprio 0
	s_barrier
	v_lshl_add_u64 v[150:151], v[182:183], 0, s[36:37]
	s_mov_b32 m0, s86
	ds_read_b128 v[110:113], v100
	ds_read_b128 v[114:117], v100 offset:1024
	ds_read_b128 v[118:121], v100 offset:2048
	ds_read_b128 v[122:125], v100 offset:3072
	ds_read_b128 v[126:129], v101
	ds_read_b128 v[132:135], v102
	ds_read_b128 v[136:139], v103
	ds_read_b128 v[140:143], v104
	global_load_lds_dwordx4 v[150:151], off
	v_lshl_add_u64 v[150:151], v[184:185], 0, s[36:37]
	s_mov_b32 m0, s87
	s_nop 0
	global_load_lds_dwordx4 v[150:151], off
	v_lshl_add_u64 v[150:151], v[186:187], 0, s[38:39]
	s_mov_b32 m0, s88
	s_nop 0
	global_load_lds_dwordx4 v[150:151], off
	v_lshl_add_u64 v[150:151], v[188:189], 0, s[38:39]
	s_mov_b32 m0, s89
	s_nop 0
	global_load_lds_dwordx4 v[150:151], off
	v_lshl_add_u64 v[150:151], v[186:187], 0, s[40:41]
	s_mov_b32 m0, s90
	s_nop 0
	global_load_lds_dwordx4 v[150:151], off
	v_lshl_add_u64 v[150:151], v[188:189], 0, s[40:41]
	s_mov_b32 m0, s91
	s_nop 0
	global_load_lds_dwordx4 v[150:151], off
	ds_read_b128 v[150:153], v99
	ds_read_b128 v[154:157], v99 offset:1024
	ds_read_b128 v[158:161], v99 offset:2048
	ds_read_b128 v[162:165], v99 offset:3072
	ds_read_b128 v[166:169], v99 offset:4096
	ds_read_b128 v[170:173], v99 offset:5120
	ds_read_b128 v[174:177], v99 offset:6144
	ds_read_b128 v[178:181], v99 offset:7168
	s_waitcnt vmcnt(6)
	s_waitcnt lgkmcnt(0)
	s_barrier
	s_setprio 1
	s_waitcnt lgkmcnt(0)
	v_mfma_f32_16x16x32_f16 v[62:65], v[150:153], v[110:113], v[62:65]
	v_mfma_f32_16x16x32_f16 v[58:61], v[158:161], v[110:113], v[58:61]
	v_mfma_f32_16x16x32_f16 v[54:57], v[166:169], v[110:113], v[54:57]
	v_mfma_f32_16x16x32_f16 v[50:53], v[174:177], v[110:113], v[50:53]
	v_mfma_f32_16x16x32_f16 v[46:49], v[150:153], v[118:121], v[46:49]
	v_mfma_f32_16x16x32_f16 v[42:45], v[158:161], v[118:121], v[42:45]
	v_mfma_f32_16x16x32_f16 v[38:41], v[166:169], v[118:121], v[38:41]
	v_mfma_f32_16x16x32_f16 v[34:37], v[174:177], v[118:121], v[34:37]
	v_mfma_f32_16x16x32_f16 v[30:33], v[150:153], v[126:129], v[30:33]
	v_mfma_f32_16x16x32_f16 v[26:29], v[158:161], v[126:129], v[26:29]
	v_mfma_f32_16x16x32_f16 v[22:25], v[166:169], v[126:129], v[22:25]
	v_mfma_f32_16x16x32_f16 v[18:21], v[174:177], v[126:129], v[18:21]
	v_mfma_f32_16x16x32_f16 v[14:17], v[150:153], v[136:139], v[14:17]
	v_mfma_f32_16x16x32_f16 v[10:13], v[158:161], v[136:139], v[10:13]
	v_mfma_f32_16x16x32_f16 v[6:9], v[166:169], v[136:139], v[6:9]
	v_mfma_f32_16x16x32_f16 v[2:5], v[174:177], v[136:139], v[2:5]
	v_mfma_f32_16x16x32_f16 v[62:65], v[154:157], v[114:117], v[62:65]
	v_mfma_f32_16x16x32_f16 v[58:61], v[162:165], v[114:117], v[58:61]
	v_mfma_f32_16x16x32_f16 v[54:57], v[170:173], v[114:117], v[54:57]
	v_mfma_f32_16x16x32_f16 v[50:53], v[178:181], v[114:117], v[50:53]
	v_mfma_f32_16x16x32_f16 v[46:49], v[154:157], v[122:125], v[46:49]
	v_mfma_f32_16x16x32_f16 v[42:45], v[162:165], v[122:125], v[42:45]
	v_mfma_f32_16x16x32_f16 v[38:41], v[170:173], v[122:125], v[38:41]
	v_mfma_f32_16x16x32_f16 v[34:37], v[178:181], v[122:125], v[34:37]
	v_mfma_f32_16x16x32_f16 v[30:33], v[154:157], v[132:135], v[30:33]
	v_mfma_f32_16x16x32_f16 v[26:29], v[162:165], v[132:135], v[26:29]
	v_mfma_f32_16x16x32_f16 v[22:25], v[170:173], v[132:135], v[22:25]
	v_mfma_f32_16x16x32_f16 v[18:21], v[178:181], v[132:135], v[18:21]
	v_mfma_f32_16x16x32_f16 v[14:17], v[154:157], v[140:143], v[14:17]
	v_mfma_f32_16x16x32_f16 v[10:13], v[162:165], v[140:143], v[10:13]
	v_mfma_f32_16x16x32_f16 v[6:9], v[170:173], v[140:143], v[6:9]
	v_mfma_f32_16x16x32_f16 v[2:5], v[178:181], v[140:143], v[2:5]
	s_setprio 0
	s_barrier
	s_add_i32 s23, s23, 3
	v_lshl_add_u64 v[74:75], v[74:75], 0, s[30:31]
	v_lshl_add_u64 v[76:77], v[76:77], 0, s[30:31]
	v_lshl_add_u64 v[78:79], v[78:79], 0, s[30:31]
	s_cmp_lt_u32 s23, 27
	v_lshl_add_u64 v[80:81], v[80:81], 0, s[30:31]
	s_cbranch_scc1 .LBB1_10
	ds_read_b128 v[74:77], v97 offset:32768
	ds_read_b128 v[78:81], v97 offset:33792
	ds_read_b128 v[88:91], v97 offset:34816
	ds_read_b128 v[98:101], v97 offset:35840
	ds_read_b128 v[102:105], v97 offset:36864
	ds_read_b128 v[106:109], v97 offset:37888
	ds_read_b128 v[110:113], v97 offset:38912
	ds_read_b128 v[114:117], v97 offset:39936
	ds_read_b128 v[118:121], v92
	ds_read_b128 v[122:125], v92 offset:1024
	ds_read_b128 v[126:129], v92 offset:2048
	ds_read_b128 v[132:135], v92 offset:3072
	ds_read_b128 v[136:139], v92 offset:4096
	ds_read_b128 v[140:143], v92 offset:5120
	ds_read_b128 v[150:153], v92 offset:6144
	ds_read_b128 v[154:157], v92 offset:7168
	s_waitcnt vmcnt(0)
	s_waitcnt lgkmcnt(0)
	s_barrier
	s_setprio 1
	s_waitcnt lgkmcnt(0)
	v_mfma_f32_16x16x32_f16 v[62:65], v[74:77], v[118:121], v[62:65]
	v_mfma_f32_16x16x32_f16 v[58:61], v[88:91], v[118:121], v[58:61]
	v_mfma_f32_16x16x32_f16 v[54:57], v[102:105], v[118:121], v[54:57]
	v_mfma_f32_16x16x32_f16 v[50:53], v[110:113], v[118:121], v[50:53]
	v_mfma_f32_16x16x32_f16 v[46:49], v[74:77], v[126:129], v[46:49]
	v_mfma_f32_16x16x32_f16 v[42:45], v[88:91], v[126:129], v[42:45]
	v_mfma_f32_16x16x32_f16 v[38:41], v[102:105], v[126:129], v[38:41]
	v_mfma_f32_16x16x32_f16 v[34:37], v[110:113], v[126:129], v[34:37]
	v_mfma_f32_16x16x32_f16 v[30:33], v[74:77], v[136:139], v[30:33]
	v_mfma_f32_16x16x32_f16 v[26:29], v[88:91], v[136:139], v[26:29]
	v_mfma_f32_16x16x32_f16 v[22:25], v[102:105], v[136:139], v[22:25]
	v_mfma_f32_16x16x32_f16 v[18:21], v[110:113], v[136:139], v[18:21]
	v_mfma_f32_16x16x32_f16 v[14:17], v[74:77], v[150:153], v[14:17]
	v_mfma_f32_16x16x32_f16 v[10:13], v[88:91], v[150:153], v[10:13]
	v_mfma_f32_16x16x32_f16 v[6:9], v[102:105], v[150:153], v[6:9]
	v_mfma_f32_16x16x32_f16 v[2:5], v[110:113], v[150:153], v[2:5]
	v_mfma_f32_16x16x32_f16 v[62:65], v[78:81], v[122:125], v[62:65]
	v_mfma_f32_16x16x32_f16 v[58:61], v[98:101], v[122:125], v[58:61]
	v_mfma_f32_16x16x32_f16 v[54:57], v[106:109], v[122:125], v[54:57]
	v_mfma_f32_16x16x32_f16 v[50:53], v[114:117], v[122:125], v[50:53]
	v_mfma_f32_16x16x32_f16 v[46:49], v[78:81], v[132:135], v[46:49]
	v_mfma_f32_16x16x32_f16 v[42:45], v[98:101], v[132:135], v[42:45]
	v_mfma_f32_16x16x32_f16 v[38:41], v[106:109], v[132:135], v[38:41]
	v_mfma_f32_16x16x32_f16 v[34:37], v[114:117], v[132:135], v[34:37]
	v_mfma_f32_16x16x32_f16 v[30:33], v[78:81], v[140:143], v[30:33]
	v_mfma_f32_16x16x32_f16 v[26:29], v[98:101], v[140:143], v[26:29]
	v_mfma_f32_16x16x32_f16 v[22:25], v[106:109], v[140:143], v[22:25]
	v_mfma_f32_16x16x32_f16 v[18:21], v[114:117], v[140:143], v[18:21]
	v_mfma_f32_16x16x32_f16 v[14:17], v[78:81], v[154:157], v[14:17]
	v_mfma_f32_16x16x32_f16 v[10:13], v[98:101], v[154:157], v[10:13]
	v_mfma_f32_16x16x32_f16 v[6:9], v[106:109], v[154:157], v[6:9]
	v_mfma_f32_16x16x32_f16 v[2:5], v[114:117], v[154:157], v[2:5]
	s_setprio 0
	s_barrier
	ds_read_b128 v[74:77], v96
	ds_read_b128 v[78:81], v96 offset:1024
	ds_read_b128 v[88:91], v96 offset:2048
	ds_read_b128 v[98:101], v96 offset:3072
	ds_read_b128 v[102:105], v96 offset:4096
	ds_read_b128 v[106:109], v96 offset:5120
	ds_read_b128 v[110:113], v96 offset:6144
	ds_read_b128 v[94:97], v96 offset:7168
	ds_read_b128 v[114:117], v92 offset:49152
	ds_read_b128 v[118:121], v92 offset:50176
	ds_read_b128 v[122:125], v92 offset:51200
	ds_read_b128 v[126:129], v92 offset:52224
	ds_read_b128 v[132:135], v92 offset:53248
	ds_read_b128 v[136:139], v92 offset:54272
	ds_read_b128 v[140:143], v92 offset:55296
	ds_read_b128 v[150:153], v92 offset:56320
	s_waitcnt lgkmcnt(0)
	s_barrier
	s_setprio 1
	s_waitcnt lgkmcnt(0)
	v_mfma_f32_16x16x32_f16 v[62:65], v[74:77], v[114:117], v[62:65]
	v_mfma_f32_16x16x32_f16 v[58:61], v[88:91], v[114:117], v[58:61]
	v_mfma_f32_16x16x32_f16 v[54:57], v[102:105], v[114:117], v[54:57]
	v_mfma_f32_16x16x32_f16 v[50:53], v[110:113], v[114:117], v[50:53]
	v_mfma_f32_16x16x32_f16 v[46:49], v[74:77], v[122:125], v[46:49]
	v_mfma_f32_16x16x32_f16 v[42:45], v[88:91], v[122:125], v[42:45]
	v_mfma_f32_16x16x32_f16 v[38:41], v[102:105], v[122:125], v[38:41]
	v_mfma_f32_16x16x32_f16 v[34:37], v[110:113], v[122:125], v[34:37]
	v_mfma_f32_16x16x32_f16 v[30:33], v[74:77], v[132:135], v[30:33]
	v_mfma_f32_16x16x32_f16 v[26:29], v[88:91], v[132:135], v[26:29]
	v_mfma_f32_16x16x32_f16 v[22:25], v[102:105], v[132:135], v[22:25]
	v_mfma_f32_16x16x32_f16 v[18:21], v[110:113], v[132:135], v[18:21]
	v_mfma_f32_16x16x32_f16 v[14:17], v[74:77], v[140:143], v[14:17]
	v_mfma_f32_16x16x32_f16 v[10:13], v[88:91], v[140:143], v[10:13]
	v_mfma_f32_16x16x32_f16 v[6:9], v[102:105], v[140:143], v[6:9]
	v_mfma_f32_16x16x32_f16 v[2:5], v[110:113], v[140:143], v[2:5]
	v_mfma_f32_16x16x32_f16 v[62:65], v[78:81], v[118:121], v[62:65]
	v_mfma_f32_16x16x32_f16 v[58:61], v[98:101], v[118:121], v[58:61]
	v_mfma_f32_16x16x32_f16 v[54:57], v[106:109], v[118:121], v[54:57]
	v_mfma_f32_16x16x32_f16 v[50:53], v[94:97], v[118:121], v[50:53]
	v_mfma_f32_16x16x32_f16 v[46:49], v[78:81], v[126:129], v[46:49]
	v_mfma_f32_16x16x32_f16 v[42:45], v[98:101], v[126:129], v[42:45]
	v_mfma_f32_16x16x32_f16 v[38:41], v[106:109], v[126:129], v[38:41]
	v_mfma_f32_16x16x32_f16 v[34:37], v[94:97], v[126:129], v[34:37]
	v_mfma_f32_16x16x32_f16 v[30:33], v[78:81], v[136:139], v[30:33]
	v_mfma_f32_16x16x32_f16 v[26:29], v[98:101], v[136:139], v[26:29]
	v_mfma_f32_16x16x32_f16 v[22:25], v[106:109], v[136:139], v[22:25]
	v_mfma_f32_16x16x32_f16 v[18:21], v[94:97], v[136:139], v[18:21]
	v_mfma_f32_16x16x32_f16 v[14:17], v[78:81], v[150:153], v[14:17]
	v_mfma_f32_16x16x32_f16 v[10:13], v[98:101], v[150:153], v[10:13]
	v_mfma_f32_16x16x32_f16 v[6:9], v[106:109], v[150:153], v[6:9]
	v_mfma_f32_16x16x32_f16 v[2:5], v[94:97], v[150:153], v[2:5]
	s_setprio 0
	s_movk_i32 s0, 0x100
	v_cmp_gt_u32_e64 s[0:1], s0, v0
	s_barrier
	s_and_saveexec_b64 s[24:25], s[0:1]
	s_cbranch_execz .LBB1_13
	s_barrier

.LBB1_112:
	s_or_b64 exec, exec, s[8:9]
	s_add_i32 s8, 0, 0x20000
	v_lshlrev_b32_e32 v4, 6, v0
	s_add_u32 s6, s12, s6
	v_and_b32_e32 v4, 0x4000, v4
	v_lshlrev_b32_e32 v5, 13, v217
	s_addc_u32 s7, s13, s7
	v_bfe_u32 v74, v0, 6, 1
	s_waitcnt vmcnt(6)
	v_and_b32_e32 v5, 0x2000, v5
	v_add3_u32 v4, 0, v4, v225
	s_add_u32 s4, s14, s4
	v_lshlrev_b32_e32 v3, 13, v74
	v_add_u32_e32 v6, s8, v225
	v_add_u32_e32 v7, 0x18000, v4
	v_add_u32_e32 v78, v4, v5
	s_addc_u32 s5, s15, s5
	v_add_u32_e32 v91, s8, v222
	v_add_u32_e32 v86, 0x19000, v78
	v_add_u32_e32 v87, 0x19400, v78
	v_add_u32_e32 v88, 0x19800, v78
	v_add_u32_e32 v89, 0x19c00, v78
	v_lshl_add_u64 v[66:67], s[6:7], 0, v[210:211]
	v_lshl_add_u64 v[68:69], s[6:7], 0, v[208:209]
	v_lshl_add_u64 v[70:71], s[4:5], 0, v[210:211]
	v_lshl_add_u64 v[72:73], s[4:5], 0, v[208:209]
	s_mov_b32 s3, -3
	v_add_u32_e32 v90, v224, v3
	s_mov_b64 s[4:5], 0x1000100
	v_add_u32_e32 v92, 0x2000, v91
	s_mov_b64 s[6:7], 0x100
	v_add_u32_e32 v93, 0x2000, v220
	s_mov_b64 s[8:9], 0x80100
	v_add_u32_e32 v94, 0x2000, v221
	v_add_u32_e32 v83, v223, v3
	s_mov_b64 s[12:13], 0x1000180
	s_mov_b64 s[14:15], 0x180
	s_mov_b64 s[16:17], 0x80180
	v_add_u32_e32 v95, v6, v3
	v_add_u32_e32 v96, v7, v5
	s_mov_b64 s[18:19], 0x1000200
	s_mov_b64 s[20:21], 0x200
	s_mov_b64 s[22:23], 0x80200
	v_mov_b32_e32 v3, v2
	v_mov_b32_e32 v4, v2
	v_mov_b32_e32 v5, v2
	v_mov_b32_e32 v6, v2
	v_mov_b32_e32 v7, v2
	v_mov_b32_e32 v8, v2
	v_mov_b32_e32 v9, v2
	v_mov_b32_e32 v10, v2
	v_mov_b32_e32 v11, v2
	v_mov_b32_e32 v12, v2
	v_mov_b32_e32 v13, v2
	v_mov_b32_e32 v14, v2
	v_mov_b32_e32 v15, v2
	v_mov_b32_e32 v16, v2
	v_mov_b32_e32 v17, v2
	v_mov_b32_e32 v18, v2
	v_mov_b32_e32 v19, v2
	v_mov_b32_e32 v20, v2
	v_mov_b32_e32 v21, v2
	v_mov_b32_e32 v22, v2
	v_mov_b32_e32 v23, v2
	v_mov_b32_e32 v24, v2
	v_mov_b32_e32 v25, v2
	v_mov_b32_e32 v26, v2
	v_mov_b32_e32 v27, v2
	v_mov_b32_e32 v28, v2
	v_mov_b32_e32 v29, v2
	v_mov_b32_e32 v30, v2
	v_mov_b32_e32 v31, v2
	v_mov_b32_e32 v32, v2
	v_mov_b32_e32 v33, v2
	v_mov_b32_e32 v34, v2
	v_mov_b32_e32 v35, v2
	v_mov_b32_e32 v36, v2
	v_mov_b32_e32 v37, v2
	v_mov_b32_e32 v38, v2
	v_mov_b32_e32 v39, v2
	v_mov_b32_e32 v40, v2
	v_mov_b32_e32 v41, v2
	v_mov_b32_e32 v42, v2
	v_mov_b32_e32 v43, v2
	v_mov_b32_e32 v44, v2
	v_mov_b32_e32 v45, v2
	v_mov_b32_e32 v46, v2
	v_mov_b32_e32 v47, v2
	v_mov_b32_e32 v48, v2
	v_mov_b32_e32 v49, v2
	v_mov_b32_e32 v50, v2
	v_mov_b32_e32 v51, v2
	v_mov_b32_e32 v52, v2
	v_mov_b32_e32 v53, v2
	v_mov_b32_e32 v54, v2
	v_mov_b32_e32 v55, v2
	v_mov_b32_e32 v56, v2
	v_mov_b32_e32 v57, v2
	v_mov_b32_e32 v58, v2
	v_mov_b32_e32 v59, v2
	v_mov_b32_e32 v60, v2
	v_mov_b32_e32 v61, v2
	v_mov_b32_e32 v62, v2
	v_mov_b32_e32 v63, v2
	v_mov_b32_e32 v64, v2
	v_mov_b32_e32 v65, v2
	s_barrier
	s_barrier
	s_nop 1
	v_readfirstlane_b32 s74, v91
	v_readfirstlane_b32 s75, v92
	v_readfirstlane_b32 s76, v220
	v_readfirstlane_b32 s77, v93
	v_readfirstlane_b32 s78, v221
	v_readfirstlane_b32 s79, v94
	v_readfirstlane_b32 s80, v75
	v_readfirstlane_b32 s81, v76
	v_readfirstlane_b32 s82, v218
	v_readfirstlane_b32 s83, v77
	v_readfirstlane_b32 s84, v79
	v_readfirstlane_b32 s85, v80
	v_readfirstlane_b32 s86, v219
	v_readfirstlane_b32 s87, v81
	v_readfirstlane_b32 s88, v82
	v_readfirstlane_b32 s89, v84
	v_readfirstlane_b32 s90, v216
	v_readfirstlane_b32 s91, v85
	v_lshl_add_u64 v[162:163], v[72:73], 0, v[202:203]
	v_lshl_add_u64 v[98:99], v[162:163], 0, s[4:5]
	s_mov_b32 m0, s74
	v_lshl_add_u64 v[164:165], v[70:71], 0, v[202:203]
	global_load_lds_dwordx4 v[98:99], off
	v_lshl_add_u64 v[98:99], v[164:165], 0, s[4:5]
	s_mov_b32 m0, s75
	v_lshl_add_u64 v[166:167], v[68:69], 0, v[202:203]
	global_load_lds_dwordx4 v[98:99], off
	v_lshl_add_u64 v[98:99], v[166:167], 0, s[6:7]
	s_mov_b32 m0, s76
	v_lshl_add_u64 v[168:169], v[66:67], 0, v[202:203]
	global_load_lds_dwordx4 v[98:99], off
	v_lshl_add_u64 v[98:99], v[168:169], 0, s[6:7]
	s_mov_b32 m0, s77
	s_nop 0
	global_load_lds_dwordx4 v[98:99], off
	v_lshl_add_u64 v[98:99], v[166:167], 0, s[8:9]
	s_mov_b32 m0, s78
	s_nop 0
	global_load_lds_dwordx4 v[98:99], off
	v_lshl_add_u64 v[98:99], v[168:169], 0, s[8:9]
	s_mov_b32 m0, s79
	s_nop 0
	global_load_lds_dwordx4 v[98:99], off
	ds_read_b128 v[98:101], v90 offset:32768
	ds_read_b128 v[102:105], v90 offset:33792
	ds_read_b128 v[106:109], v90 offset:34816
	ds_read_b128 v[110:113], v90 offset:35840
	ds_read_b128 v[114:117], v90 offset:36864
	ds_read_b128 v[118:121], v90 offset:37888
	ds_read_b128 v[122:125], v90 offset:38912
	ds_read_b128 v[126:129], v90 offset:39936
	ds_read_b128 v[130:133], v78
	ds_read_b128 v[134:137], v78 offset:1024
	ds_read_b128 v[138:141], v78 offset:2048
	ds_read_b128 v[142:145], v78 offset:3072
	ds_read_b128 v[146:149], v78 offset:4096
	ds_read_b128 v[150:153], v78 offset:5120
	ds_read_b128 v[154:157], v78 offset:6144
	ds_read_b128 v[158:161], v78 offset:7168
	s_waitcnt vmcnt(6)
	s_waitcnt lgkmcnt(0)
	s_barrier
	s_setprio 1
	s_waitcnt lgkmcnt(0)
	v_mfma_f32_16x16x32_f16 v[62:65], v[98:101], v[130:133], v[62:65]
	s_lshl_b32 s60, s66, 16
	s_add_u32 s62, s58, s60
	s_addc_u32 s63, s59, 0
	s_lshl_b32 s61, s66, 15
	s_add_u32 s64, s52, s61
	s_addc_u32 s65, s53, 0
	v_lshlrev_b32_e32 v254, 5, v0
	v_lshlrev_b32_e32 v255, 4, v0
	global_load_dwordx4 v[230:233], v254, s[62:63] nt
	v_mfma_f32_16x16x32_f16 v[58:61], v[106:109], v[130:133], v[58:61]
	global_load_dwordx4 v[234:237], v254, s[62:63] offset:16 nt
	v_mfma_f32_16x16x32_f16 v[54:57], v[114:117], v[130:133], v[54:57]
	s_add_u32 s62, s62, 0x4000
	s_addc_u32 s63, s63, 0
	global_load_dwordx4 v[238:241], v254, s[62:63] nt
	v_mfma_f32_16x16x32_f16 v[50:53], v[122:125], v[130:133], v[50:53]
	global_load_dwordx4 v[242:245], v254, s[62:63] offset:16 nt
	v_mfma_f32_16x16x32_f16 v[46:49], v[98:101], v[138:141], v[46:49]
	s_add_u32 s62, s62, 0x4000
	s_addc_u32 s63, s63, 0
	global_load_dwordx4 v[246:249], v254, s[62:63] nt
	v_mfma_f32_16x16x32_f16 v[42:45], v[106:109], v[138:141], v[42:45]
	global_load_dwordx4 v[250:253], v254, s[62:63] offset:16 nt
	v_mfma_f32_16x16x32_f16 v[38:41], v[114:117], v[138:141], v[38:41]
	s_add_u32 s62, s62, 0x4000
	s_addc_u32 s63, s63, 0
	global_load_dwordx4 v[190:193], v254, s[62:63] nt
	v_mfma_f32_16x16x32_f16 v[34:37], v[122:125], v[138:141], v[34:37]
	global_load_dwordx4 v[194:197], v254, s[62:63] offset:16 nt
	v_mfma_f32_16x16x32_f16 v[30:33], v[98:101], v[146:149], v[30:33]
	v_mfma_f32_16x16x32_f16 v[26:29], v[106:109], v[146:149], v[26:29]
	v_mfma_f32_16x16x32_f16 v[22:25], v[114:117], v[146:149], v[22:25]
	v_mfma_f32_16x16x32_f16 v[18:21], v[122:125], v[146:149], v[18:21]
	v_mfma_f32_16x16x32_f16 v[14:17], v[98:101], v[154:157], v[14:17]
	v_mfma_f32_16x16x32_f16 v[10:13], v[106:109], v[154:157], v[10:13]
	v_mfma_f32_16x16x32_f16 v[6:9], v[114:117], v[154:157], v[6:9]
	v_mfma_f32_16x16x32_f16 v[2:5], v[122:125], v[154:157], v[2:5]
	v_mfma_f32_16x16x32_f16 v[62:65], v[102:105], v[134:137], v[62:65]
	v_mfma_f32_16x16x32_f16 v[58:61], v[110:113], v[134:137], v[58:61]
	v_mfma_f32_16x16x32_f16 v[54:57], v[118:121], v[134:137], v[54:57]
	v_mfma_f32_16x16x32_f16 v[50:53], v[126:129], v[134:137], v[50:53]
	v_mfma_f32_16x16x32_f16 v[46:49], v[102:105], v[142:145], v[46:49]
	v_mfma_f32_16x16x32_f16 v[42:45], v[110:113], v[142:145], v[42:45]
	v_mfma_f32_16x16x32_f16 v[38:41], v[118:121], v[142:145], v[38:41]
	v_mfma_f32_16x16x32_f16 v[34:37], v[126:129], v[142:145], v[34:37]
	v_mfma_f32_16x16x32_f16 v[30:33], v[102:105], v[150:153], v[30:33]
	v_mfma_f32_16x16x32_f16 v[26:29], v[110:113], v[150:153], v[26:29]
	v_mfma_f32_16x16x32_f16 v[22:25], v[118:121], v[150:153], v[22:25]
	v_mfma_f32_16x16x32_f16 v[18:21], v[126:129], v[150:153], v[18:21]
	v_mfma_f32_16x16x32_f16 v[14:17], v[102:105], v[158:161], v[14:17]
	v_mfma_f32_16x16x32_f16 v[10:13], v[110:113], v[158:161], v[10:13]
	v_mfma_f32_16x16x32_f16 v[6:9], v[118:121], v[158:161], v[6:9]
	v_mfma_f32_16x16x32_f16 v[2:5], v[126:129], v[158:161], v[2:5]
	s_setprio 0
	s_barrier
	v_lshl_add_u64 v[130:131], v[162:163], 0, s[12:13]
	s_mov_b32 m0, s80
	ds_read_b128 v[98:101], v78 offset:49152
	ds_read_b128 v[102:105], v78 offset:50176
	ds_read_b128 v[106:109], v78 offset:51200
	ds_read_b128 v[110:113], v78 offset:52224
	ds_read_b128 v[114:117], v78 offset:53248
	ds_read_b128 v[118:121], v78 offset:54272
	ds_read_b128 v[122:125], v78 offset:55296
	ds_read_b128 v[126:129], v78 offset:56320
	global_load_lds_dwordx4 v[130:131], off
	v_lshl_add_u64 v[130:131], v[164:165], 0, s[12:13]
	s_mov_b32 m0, s81
	s_nop 0
	global_load_lds_dwordx4 v[130:131], off
	v_lshl_add_u64 v[130:131], v[166:167], 0, s[14:15]
	s_mov_b32 m0, s82
	s_nop 0
	global_load_lds_dwordx4 v[130:131], off
	v_lshl_add_u64 v[130:131], v[168:169], 0, s[14:15]
	s_mov_b32 m0, s83
	s_nop 0
	global_load_lds_dwordx4 v[130:131], off
	v_lshl_add_u64 v[130:131], v[166:167], 0, s[16:17]
	s_mov_b32 m0, s84
	s_nop 0
	global_load_lds_dwordx4 v[130:131], off
	v_lshl_add_u64 v[130:131], v[168:169], 0, s[16:17]
	s_mov_b32 m0, s85
	s_nop 0
	global_load_lds_dwordx4 v[130:131], off
	ds_read_b128 v[130:133], v83
	ds_read_b128 v[134:137], v83 offset:1024
	ds_read_b128 v[138:141], v83 offset:2048
	ds_read_b128 v[142:145], v83 offset:3072
	ds_read_b128 v[146:149], v83 offset:4096
	ds_read_b128 v[150:153], v83 offset:5120
	ds_read_b128 v[154:157], v83 offset:6144
	ds_read_b128 v[158:161], v83 offset:7168
	s_waitcnt vmcnt(14)
	s_waitcnt lgkmcnt(0)
	s_barrier
	s_setprio 1
	s_waitcnt lgkmcnt(0)
	v_mfma_f32_16x16x32_f16 v[62:65], v[130:133], v[98:101], v[62:65]
	v_mfma_f32_16x16x32_f16 v[58:61], v[138:141], v[98:101], v[58:61]
	v_mfma_f32_16x16x32_f16 v[54:57], v[146:149], v[98:101], v[54:57]
	v_mfma_f32_16x16x32_f16 v[50:53], v[154:157], v[98:101], v[50:53]
	v_mfma_f32_16x16x32_f16 v[46:49], v[130:133], v[106:109], v[46:49]
	v_mfma_f32_16x16x32_f16 v[42:45], v[138:141], v[106:109], v[42:45]
	v_mfma_f32_16x16x32_f16 v[38:41], v[146:149], v[106:109], v[38:41]
	v_mfma_f32_16x16x32_f16 v[34:37], v[154:157], v[106:109], v[34:37]
	v_mfma_f32_16x16x32_f16 v[30:33], v[130:133], v[114:117], v[30:33]
	v_mfma_f32_16x16x32_f16 v[26:29], v[138:141], v[114:117], v[26:29]
	v_mfma_f32_16x16x32_f16 v[22:25], v[146:149], v[114:117], v[22:25]
	v_mfma_f32_16x16x32_f16 v[18:21], v[154:157], v[114:117], v[18:21]
	v_mfma_f32_16x16x32_f16 v[14:17], v[130:133], v[122:125], v[14:17]
	v_mfma_f32_16x16x32_f16 v[10:13], v[138:141], v[122:125], v[10:13]
	v_mfma_f32_16x16x32_f16 v[6:9], v[146:149], v[122:125], v[6:9]
	v_mfma_f32_16x16x32_f16 v[2:5], v[154:157], v[122:125], v[2:5]
	v_mfma_f32_16x16x32_f16 v[62:65], v[134:137], v[102:105], v[62:65]
	v_mfma_f32_16x16x32_f16 v[58:61], v[142:145], v[102:105], v[58:61]
	v_mfma_f32_16x16x32_f16 v[54:57], v[150:153], v[102:105], v[54:57]
	v_mfma_f32_16x16x32_f16 v[50:53], v[158:161], v[102:105], v[50:53]
	v_mfma_f32_16x16x32_f16 v[46:49], v[134:137], v[110:113], v[46:49]
	v_mfma_f32_16x16x32_f16 v[42:45], v[142:145], v[110:113], v[42:45]
	v_mfma_f32_16x16x32_f16 v[38:41], v[150:153], v[110:113], v[38:41]
	v_mfma_f32_16x16x32_f16 v[34:37], v[158:161], v[110:113], v[34:37]
	v_mfma_f32_16x16x32_f16 v[30:33], v[134:137], v[118:121], v[30:33]
	v_mfma_f32_16x16x32_f16 v[26:29], v[142:145], v[118:121], v[26:29]
	v_mfma_f32_16x16x32_f16 v[22:25], v[150:153], v[118:121], v[22:25]
	v_mfma_f32_16x16x32_f16 v[18:21], v[158:161], v[118:121], v[18:21]
	v_mfma_f32_16x16x32_f16 v[14:17], v[134:137], v[126:129], v[14:17]
	v_mfma_f32_16x16x32_f16 v[10:13], v[142:145], v[126:129], v[10:13]
	v_mfma_f32_16x16x32_f16 v[6:9], v[150:153], v[126:129], v[6:9]
	v_mfma_f32_16x16x32_f16 v[2:5], v[158:161], v[126:129], v[2:5]
	s_setprio 0
	s_barrier
	v_lshl_add_u64 v[130:131], v[162:163], 0, s[18:19]
	s_mov_b32 m0, s86
	ds_read_b128 v[98:101], v96
	ds_read_b128 v[102:105], v96 offset:1024
	ds_read_b128 v[106:109], v96 offset:2048
	ds_read_b128 v[110:113], v96 offset:3072
	ds_read_b128 v[114:117], v86
	ds_read_b128 v[118:121], v87
	ds_read_b128 v[122:125], v88
	ds_read_b128 v[126:129], v89
	global_load_lds_dwordx4 v[130:131], off
	v_lshl_add_u64 v[130:131], v[164:165], 0, s[18:19]
	s_mov_b32 m0, s87
	s_nop 0
	global_load_lds_dwordx4 v[130:131], off
	v_lshl_add_u64 v[130:131], v[166:167], 0, s[20:21]
	s_mov_b32 m0, s88
	s_nop 0
	global_load_lds_dwordx4 v[130:131], off
	v_lshl_add_u64 v[130:131], v[168:169], 0, s[20:21]
	s_mov_b32 m0, s89
	s_nop 0
	global_load_lds_dwordx4 v[130:131], off
	v_lshl_add_u64 v[130:131], v[166:167], 0, s[22:23]
	s_mov_b32 m0, s90
	s_nop 0
	global_load_lds_dwordx4 v[130:131], off
	v_lshl_add_u64 v[130:131], v[168:169], 0, s[22:23]
	s_mov_b32 m0, s91
	s_nop 0
	global_load_lds_dwordx4 v[130:131], off
	ds_read_b128 v[130:133], v95
	ds_read_b128 v[134:137], v95 offset:1024
	ds_read_b128 v[138:141], v95 offset:2048
	ds_read_b128 v[142:145], v95 offset:3072
	ds_read_b128 v[146:149], v95 offset:4096
	ds_read_b128 v[150:153], v95 offset:5120
	ds_read_b128 v[154:157], v95 offset:6144
	ds_read_b128 v[158:161], v95 offset:7168
	s_waitcnt vmcnt(6)
	s_waitcnt lgkmcnt(0)
	s_barrier
	s_setprio 1
	s_waitcnt lgkmcnt(0)
	v_mfma_f32_16x16x32_f16 v[62:65], v[130:133], v[98:101], v[62:65]
	v_cvt_pk_f16_f32 v230, v230, v231
	v_mfma_f32_16x16x32_f16 v[58:61], v[138:141], v[98:101], v[58:61]
	v_cvt_pk_f16_f32 v231, v232, v233
	v_mfma_f32_16x16x32_f16 v[54:57], v[146:149], v[98:101], v[54:57]
	v_cvt_pk_f16_f32 v232, v234, v235
	v_mfma_f32_16x16x32_f16 v[50:53], v[154:157], v[98:101], v[50:53]
	v_cvt_pk_f16_f32 v233, v236, v237
	v_mfma_f32_16x16x32_f16 v[46:49], v[130:133], v[106:109], v[46:49]
	global_store_dwordx4 v255, v[230:233], s[64:65]
	v_mfma_f32_16x16x32_f16 v[42:45], v[138:141], v[106:109], v[42:45]
	s_add_u32 s64, s64, 0x2000
	s_addc_u32 s65, s65, 0
	v_mfma_f32_16x16x32_f16 v[38:41], v[146:149], v[106:109], v[38:41]
	v_cvt_pk_f16_f32 v238, v238, v239
	v_mfma_f32_16x16x32_f16 v[34:37], v[154:157], v[106:109], v[34:37]
	v_cvt_pk_f16_f32 v239, v240, v241
	v_mfma_f32_16x16x32_f16 v[30:33], v[130:133], v[114:117], v[30:33]
	v_cvt_pk_f16_f32 v240, v242, v243
	v_mfma_f32_16x16x32_f16 v[26:29], v[138:141], v[114:117], v[26:29]
	v_cvt_pk_f16_f32 v241, v244, v245
	v_mfma_f32_16x16x32_f16 v[22:25], v[146:149], v[114:117], v[22:25]
	global_store_dwordx4 v255, v[238:241], s[64:65]
	v_mfma_f32_16x16x32_f16 v[18:21], v[154:157], v[114:117], v[18:21]
	s_add_u32 s64, s64, 0x2000
	s_addc_u32 s65, s65, 0
	v_mfma_f32_16x16x32_f16 v[14:17], v[130:133], v[122:125], v[14:17]
	v_cvt_pk_f16_f32 v246, v246, v247
	v_mfma_f32_16x16x32_f16 v[10:13], v[138:141], v[122:125], v[10:13]
	v_cvt_pk_f16_f32 v247, v248, v249
	v_mfma_f32_16x16x32_f16 v[6:9], v[146:149], v[122:125], v[6:9]
	v_cvt_pk_f16_f32 v248, v250, v251
	v_mfma_f32_16x16x32_f16 v[2:5], v[154:157], v[122:125], v[2:5]
	v_cvt_pk_f16_f32 v249, v252, v253
	v_mfma_f32_16x16x32_f16 v[62:65], v[134:137], v[102:105], v[62:65]
	global_store_dwordx4 v255, v[246:249], s[64:65]
	v_mfma_f32_16x16x32_f16 v[58:61], v[142:145], v[102:105], v[58:61]
	s_add_u32 s64, s64, 0x2000
	s_addc_u32 s65, s65, 0
	v_mfma_f32_16x16x32_f16 v[54:57], v[150:153], v[102:105], v[54:57]
	v_cvt_pk_f16_f32 v190, v190, v191
	v_mfma_f32_16x16x32_f16 v[50:53], v[158:161], v[102:105], v[50:53]
	v_cvt_pk_f16_f32 v191, v192, v193
	v_mfma_f32_16x16x32_f16 v[46:49], v[134:137], v[110:113], v[46:49]
	v_cvt_pk_f16_f32 v192, v194, v195
	v_mfma_f32_16x16x32_f16 v[42:45], v[142:145], v[110:113], v[42:45]
	v_cvt_pk_f16_f32 v193, v196, v197
	v_mfma_f32_16x16x32_f16 v[38:41], v[150:153], v[110:113], v[38:41]
	global_store_dwordx4 v255, v[190:193], s[64:65]
	v_mfma_f32_16x16x32_f16 v[34:37], v[158:161], v[110:113], v[34:37]
	v_mfma_f32_16x16x32_f16 v[30:33], v[134:137], v[118:121], v[30:33]
	v_mfma_f32_16x16x32_f16 v[26:29], v[142:145], v[118:121], v[26:29]
	v_mfma_f32_16x16x32_f16 v[22:25], v[150:153], v[118:121], v[22:25]
	v_mfma_f32_16x16x32_f16 v[18:21], v[158:161], v[118:121], v[18:21]
	v_mfma_f32_16x16x32_f16 v[14:17], v[134:137], v[126:129], v[14:17]
	v_mfma_f32_16x16x32_f16 v[10:13], v[142:145], v[126:129], v[10:13]
	v_mfma_f32_16x16x32_f16 v[6:9], v[150:153], v[126:129], v[6:9]
	v_mfma_f32_16x16x32_f16 v[2:5], v[158:161], v[126:129], v[2:5]
	s_setprio 0
	s_barrier
	s_add_i32 s3, s3, 3
	v_lshl_add_u64 v[66:67], v[66:67], 0, s[14:15]
	v_lshl_add_u64 v[68:69], v[68:69], 0, s[14:15]
	v_lshl_add_u64 v[70:71], v[70:71], 0, s[14:15]
	v_lshl_add_u64 v[72:73], v[72:73], 0, s[14:15]
.LBB1_113:
	v_lshl_add_u64 v[162:163], v[72:73], 0, v[202:203]
	v_lshl_add_u64 v[98:99], v[162:163], 0, s[4:5]
	s_mov_b32 m0, s74
	v_lshl_add_u64 v[164:165], v[70:71], 0, v[202:203]
	global_load_lds_dwordx4 v[98:99], off
	v_lshl_add_u64 v[98:99], v[164:165], 0, s[4:5]
	s_mov_b32 m0, s75
	v_lshl_add_u64 v[166:167], v[68:69], 0, v[202:203]
	global_load_lds_dwordx4 v[98:99], off
	v_lshl_add_u64 v[98:99], v[166:167], 0, s[6:7]
	s_mov_b32 m0, s76
	v_lshl_add_u64 v[168:169], v[66:67], 0, v[202:203]
	global_load_lds_dwordx4 v[98:99], off
	v_lshl_add_u64 v[98:99], v[168:169], 0, s[6:7]
	s_mov_b32 m0, s77
	s_nop 0
	global_load_lds_dwordx4 v[98:99], off
	v_lshl_add_u64 v[98:99], v[166:167], 0, s[8:9]
	s_mov_b32 m0, s78
	s_nop 0
	global_load_lds_dwordx4 v[98:99], off
	v_lshl_add_u64 v[98:99], v[168:169], 0, s[8:9]
	s_mov_b32 m0, s79
	s_nop 0
	global_load_lds_dwordx4 v[98:99], off
	ds_read_b128 v[98:101], v90 offset:32768
	ds_read_b128 v[102:105], v90 offset:33792
	ds_read_b128 v[106:109], v90 offset:34816
	ds_read_b128 v[110:113], v90 offset:35840
	ds_read_b128 v[114:117], v90 offset:36864
	ds_read_b128 v[118:121], v90 offset:37888
	ds_read_b128 v[122:125], v90 offset:38912
	ds_read_b128 v[126:129], v90 offset:39936
	ds_read_b128 v[130:133], v78
	ds_read_b128 v[134:137], v78 offset:1024
	ds_read_b128 v[138:141], v78 offset:2048
	ds_read_b128 v[142:145], v78 offset:3072
	ds_read_b128 v[146:149], v78 offset:4096
	ds_read_b128 v[150:153], v78 offset:5120
	ds_read_b128 v[154:157], v78 offset:6144
	ds_read_b128 v[158:161], v78 offset:7168
	s_waitcnt vmcnt(6)
	s_waitcnt lgkmcnt(0)
	s_barrier
	s_setprio 1
	s_waitcnt lgkmcnt(0)
	v_mfma_f32_16x16x32_f16 v[62:65], v[98:101], v[130:133], v[62:65]
	v_mfma_f32_16x16x32_f16 v[58:61], v[106:109], v[130:133], v[58:61]
	v_mfma_f32_16x16x32_f16 v[54:57], v[114:117], v[130:133], v[54:57]
	v_mfma_f32_16x16x32_f16 v[50:53], v[122:125], v[130:133], v[50:53]
	v_mfma_f32_16x16x32_f16 v[46:49], v[98:101], v[138:141], v[46:49]
	v_mfma_f32_16x16x32_f16 v[42:45], v[106:109], v[138:141], v[42:45]
	v_mfma_f32_16x16x32_f16 v[38:41], v[114:117], v[138:141], v[38:41]
	v_mfma_f32_16x16x32_f16 v[34:37], v[122:125], v[138:141], v[34:37]
	v_mfma_f32_16x16x32_f16 v[30:33], v[98:101], v[146:149], v[30:33]
	v_mfma_f32_16x16x32_f16 v[26:29], v[106:109], v[146:149], v[26:29]
	v_mfma_f32_16x16x32_f16 v[22:25], v[114:117], v[146:149], v[22:25]
	v_mfma_f32_16x16x32_f16 v[18:21], v[122:125], v[146:149], v[18:21]
	v_mfma_f32_16x16x32_f16 v[14:17], v[98:101], v[154:157], v[14:17]
	v_mfma_f32_16x16x32_f16 v[10:13], v[106:109], v[154:157], v[10:13]
	v_mfma_f32_16x16x32_f16 v[6:9], v[114:117], v[154:157], v[6:9]
	v_mfma_f32_16x16x32_f16 v[2:5], v[122:125], v[154:157], v[2:5]
	v_mfma_f32_16x16x32_f16 v[62:65], v[102:105], v[134:137], v[62:65]
	v_mfma_f32_16x16x32_f16 v[58:61], v[110:113], v[134:137], v[58:61]
	v_mfma_f32_16x16x32_f16 v[54:57], v[118:121], v[134:137], v[54:57]
	v_mfma_f32_16x16x32_f16 v[50:53], v[126:129], v[134:137], v[50:53]
	v_mfma_f32_16x16x32_f16 v[46:49], v[102:105], v[142:145], v[46:49]
	v_mfma_f32_16x16x32_f16 v[42:45], v[110:113], v[142:145], v[42:45]
	v_mfma_f32_16x16x32_f16 v[38:41], v[118:121], v[142:145], v[38:41]
	v_mfma_f32_16x16x32_f16 v[34:37], v[126:129], v[142:145], v[34:37]
	v_mfma_f32_16x16x32_f16 v[30:33], v[102:105], v[150:153], v[30:33]
	v_mfma_f32_16x16x32_f16 v[26:29], v[110:113], v[150:153], v[26:29]
	v_mfma_f32_16x16x32_f16 v[22:25], v[118:121], v[150:153], v[22:25]
	v_mfma_f32_16x16x32_f16 v[18:21], v[126:129], v[150:153], v[18:21]
	v_mfma_f32_16x16x32_f16 v[14:17], v[102:105], v[158:161], v[14:17]
	v_mfma_f32_16x16x32_f16 v[10:13], v[110:113], v[158:161], v[10:13]
	v_mfma_f32_16x16x32_f16 v[6:9], v[118:121], v[158:161], v[6:9]
	v_mfma_f32_16x16x32_f16 v[2:5], v[126:129], v[158:161], v[2:5]
	s_setprio 0
	s_barrier
	v_lshl_add_u64 v[130:131], v[162:163], 0, s[12:13]
	s_mov_b32 m0, s80
	ds_read_b128 v[98:101], v78 offset:49152
	ds_read_b128 v[102:105], v78 offset:50176
	ds_read_b128 v[106:109], v78 offset:51200
	ds_read_b128 v[110:113], v78 offset:52224
	ds_read_b128 v[114:117], v78 offset:53248
	ds_read_b128 v[118:121], v78 offset:54272
	ds_read_b128 v[122:125], v78 offset:55296
	ds_read_b128 v[126:129], v78 offset:56320
	global_load_lds_dwordx4 v[130:131], off
	v_lshl_add_u64 v[130:131], v[164:165], 0, s[12:13]
	s_mov_b32 m0, s81
	s_nop 0
	global_load_lds_dwordx4 v[130:131], off
	v_lshl_add_u64 v[130:131], v[166:167], 0, s[14:15]
	s_mov_b32 m0, s82
	s_nop 0
	global_load_lds_dwordx4 v[130:131], off
	v_lshl_add_u64 v[130:131], v[168:169], 0, s[14:15]
	s_mov_b32 m0, s83
	s_nop 0
	global_load_lds_dwordx4 v[130:131], off
	v_lshl_add_u64 v[130:131], v[166:167], 0, s[16:17]
	s_mov_b32 m0, s84
	s_nop 0
	global_load_lds_dwordx4 v[130:131], off
	v_lshl_add_u64 v[130:131], v[168:169], 0, s[16:17]
	s_mov_b32 m0, s85
	s_nop 0
	global_load_lds_dwordx4 v[130:131], off
	ds_read_b128 v[130:133], v83
	ds_read_b128 v[134:137], v83 offset:1024
	ds_read_b128 v[138:141], v83 offset:2048
	ds_read_b128 v[142:145], v83 offset:3072
	ds_read_b128 v[146:149], v83 offset:4096
	ds_read_b128 v[150:153], v83 offset:5120
	ds_read_b128 v[154:157], v83 offset:6144
	ds_read_b128 v[158:161], v83 offset:7168
	s_waitcnt vmcnt(6)
	s_waitcnt lgkmcnt(0)
	s_barrier
	s_setprio 1
	s_waitcnt lgkmcnt(0)
	v_mfma_f32_16x16x32_f16 v[62:65], v[130:133], v[98:101], v[62:65]
	v_mfma_f32_16x16x32_f16 v[58:61], v[138:141], v[98:101], v[58:61]
	v_mfma_f32_16x16x32_f16 v[54:57], v[146:149], v[98:101], v[54:57]
	v_mfma_f32_16x16x32_f16 v[50:53], v[154:157], v[98:101], v[50:53]
	v_mfma_f32_16x16x32_f16 v[46:49], v[130:133], v[106:109], v[46:49]
	v_mfma_f32_16x16x32_f16 v[42:45], v[138:141], v[106:109], v[42:45]
	v_mfma_f32_16x16x32_f16 v[38:41], v[146:149], v[106:109], v[38:41]
	v_mfma_f32_16x16x32_f16 v[34:37], v[154:157], v[106:109], v[34:37]
	v_mfma_f32_16x16x32_f16 v[30:33], v[130:133], v[114:117], v[30:33]
	v_mfma_f32_16x16x32_f16 v[26:29], v[138:141], v[114:117], v[26:29]
	v_mfma_f32_16x16x32_f16 v[22:25], v[146:149], v[114:117], v[22:25]
	v_mfma_f32_16x16x32_f16 v[18:21], v[154:157], v[114:117], v[18:21]
	v_mfma_f32_16x16x32_f16 v[14:17], v[130:133], v[122:125], v[14:17]
	v_mfma_f32_16x16x32_f16 v[10:13], v[138:141], v[122:125], v[10:13]
	v_mfma_f32_16x16x32_f16 v[6:9], v[146:149], v[122:125], v[6:9]
	v_mfma_f32_16x16x32_f16 v[2:5], v[154:157], v[122:125], v[2:5]
	v_mfma_f32_16x16x32_f16 v[62:65], v[134:137], v[102:105], v[62:65]
	v_mfma_f32_16x16x32_f16 v[58:61], v[142:145], v[102:105], v[58:61]
	v_mfma_f32_16x16x32_f16 v[54:57], v[150:153], v[102:105], v[54:57]
	v_mfma_f32_16x16x32_f16 v[50:53], v[158:161], v[102:105], v[50:53]
	v_mfma_f32_16x16x32_f16 v[46:49], v[134:137], v[110:113], v[46:49]
	v_mfma_f32_16x16x32_f16 v[42:45], v[142:145], v[110:113], v[42:45]
	v_mfma_f32_16x16x32_f16 v[38:41], v[150:153], v[110:113], v[38:41]
	v_mfma_f32_16x16x32_f16 v[34:37], v[158:161], v[110:113], v[34:37]
	v_mfma_f32_16x16x32_f16 v[30:33], v[134:137], v[118:121], v[30:33]
	v_mfma_f32_16x16x32_f16 v[26:29], v[142:145], v[118:121], v[26:29]
	v_mfma_f32_16x16x32_f16 v[22:25], v[150:153], v[118:121], v[22:25]
	v_mfma_f32_16x16x32_f16 v[18:21], v[158:161], v[118:121], v[18:21]
	v_mfma_f32_16x16x32_f16 v[14:17], v[134:137], v[126:129], v[14:17]
	v_mfma_f32_16x16x32_f16 v[10:13], v[142:145], v[126:129], v[10:13]
	v_mfma_f32_16x16x32_f16 v[6:9], v[150:153], v[126:129], v[6:9]
	v_mfma_f32_16x16x32_f16 v[2:5], v[158:161], v[126:129], v[2:5]
	s_setprio 0
	s_barrier
	v_lshl_add_u64 v[130:131], v[162:163], 0, s[18:19]
	s_mov_b32 m0, s86
	ds_read_b128 v[98:101], v96
	ds_read_b128 v[102:105], v96 offset:1024
	ds_read_b128 v[106:109], v96 offset:2048
	ds_read_b128 v[110:113], v96 offset:3072
	ds_read_b128 v[114:117], v86
	ds_read_b128 v[118:121], v87
	ds_read_b128 v[122:125], v88
	ds_read_b128 v[126:129], v89
	global_load_lds_dwordx4 v[130:131], off
	v_lshl_add_u64 v[130:131], v[164:165], 0, s[18:19]
	s_mov_b32 m0, s87
	s_nop 0
	global_load_lds_dwordx4 v[130:131], off
	v_lshl_add_u64 v[130:131], v[166:167], 0, s[20:21]
	s_mov_b32 m0, s88
	s_nop 0
	global_load_lds_dwordx4 v[130:131], off
	v_lshl_add_u64 v[130:131], v[168:169], 0, s[20:21]
	s_mov_b32 m0, s89
	s_nop 0
	global_load_lds_dwordx4 v[130:131], off
	v_lshl_add_u64 v[130:131], v[166:167], 0, s[22:23]
	s_mov_b32 m0, s90
	s_nop 0
	global_load_lds_dwordx4 v[130:131], off
	v_lshl_add_u64 v[130:131], v[168:169], 0, s[22:23]
	s_mov_b32 m0, s91
	s_nop 0
	global_load_lds_dwordx4 v[130:131], off
	ds_read_b128 v[130:133], v95
	ds_read_b128 v[134:137], v95 offset:1024
	ds_read_b128 v[138:141], v95 offset:2048
	ds_read_b128 v[142:145], v95 offset:3072
	ds_read_b128 v[146:149], v95 offset:4096
	ds_read_b128 v[150:153], v95 offset:5120
	ds_read_b128 v[154:157], v95 offset:6144
	ds_read_b128 v[158:161], v95 offset:7168
	s_waitcnt vmcnt(6)
	s_waitcnt lgkmcnt(0)
	s_barrier
	s_setprio 1
	s_waitcnt lgkmcnt(0)
	v_mfma_f32_16x16x32_f16 v[62:65], v[130:133], v[98:101], v[62:65]
	v_mfma_f32_16x16x32_f16 v[58:61], v[138:141], v[98:101], v[58:61]
	v_mfma_f32_16x16x32_f16 v[54:57], v[146:149], v[98:101], v[54:57]
	v_mfma_f32_16x16x32_f16 v[50:53], v[154:157], v[98:101], v[50:53]
	v_mfma_f32_16x16x32_f16 v[46:49], v[130:133], v[106:109], v[46:49]
	v_mfma_f32_16x16x32_f16 v[42:45], v[138:141], v[106:109], v[42:45]
	v_mfma_f32_16x16x32_f16 v[38:41], v[146:149], v[106:109], v[38:41]
	v_mfma_f32_16x16x32_f16 v[34:37], v[154:157], v[106:109], v[34:37]
	v_mfma_f32_16x16x32_f16 v[30:33], v[130:133], v[114:117], v[30:33]
	v_mfma_f32_16x16x32_f16 v[26:29], v[138:141], v[114:117], v[26:29]
	v_mfma_f32_16x16x32_f16 v[22:25], v[146:149], v[114:117], v[22:25]
	v_mfma_f32_16x16x32_f16 v[18:21], v[154:157], v[114:117], v[18:21]
	v_mfma_f32_16x16x32_f16 v[14:17], v[130:133], v[122:125], v[14:17]
	v_mfma_f32_16x16x32_f16 v[10:13], v[138:141], v[122:125], v[10:13]
	v_mfma_f32_16x16x32_f16 v[6:9], v[146:149], v[122:125], v[6:9]
	v_mfma_f32_16x16x32_f16 v[2:5], v[154:157], v[122:125], v[2:5]
	v_mfma_f32_16x16x32_f16 v[62:65], v[134:137], v[102:105], v[62:65]
	v_mfma_f32_16x16x32_f16 v[58:61], v[142:145], v[102:105], v[58:61]
	v_mfma_f32_16x16x32_f16 v[54:57], v[150:153], v[102:105], v[54:57]
	v_mfma_f32_16x16x32_f16 v[50:53], v[158:161], v[102:105], v[50:53]
	v_mfma_f32_16x16x32_f16 v[46:49], v[134:137], v[110:113], v[46:49]
	v_mfma_f32_16x16x32_f16 v[42:45], v[142:145], v[110:113], v[42:45]
	v_mfma_f32_16x16x32_f16 v[38:41], v[150:153], v[110:113], v[38:41]
	v_mfma_f32_16x16x32_f16 v[34:37], v[158:161], v[110:113], v[34:37]
	v_mfma_f32_16x16x32_f16 v[30:33], v[134:137], v[118:121], v[30:33]
	v_mfma_f32_16x16x32_f16 v[26:29], v[142:145], v[118:121], v[26:29]
	v_mfma_f32_16x16x32_f16 v[22:25], v[150:153], v[118:121], v[22:25]
	v_mfma_f32_16x16x32_f16 v[18:21], v[158:161], v[118:121], v[18:21]
	v_mfma_f32_16x16x32_f16 v[14:17], v[134:137], v[126:129], v[14:17]
	v_mfma_f32_16x16x32_f16 v[10:13], v[142:145], v[126:129], v[10:13]
	v_mfma_f32_16x16x32_f16 v[6:9], v[150:153], v[126:129], v[6:9]
	v_mfma_f32_16x16x32_f16 v[2:5], v[158:161], v[126:129], v[2:5]
	s_setprio 0
	s_barrier
	s_add_i32 s3, s3, 3
	v_lshl_add_u64 v[66:67], v[66:67], 0, s[14:15]
	v_lshl_add_u64 v[68:69], v[68:69], 0, s[14:15]
	v_lshl_add_u64 v[70:71], v[70:71], 0, s[14:15]
	s_cmp_lt_u32 s3, 27
	v_lshl_add_u64 v[72:73], v[72:73], 0, s[14:15]
	s_cbranch_scc1 .LBB1_113
	ds_read_b128 v[66:69], v90 offset:32768
	ds_read_b128 v[70:73], v90 offset:33792
	ds_read_b128 v[84:87], v90 offset:34816
	ds_read_b128 v[92:95], v90 offset:35840
	ds_read_b128 v[96:99], v90 offset:36864
	ds_read_b128 v[100:103], v90 offset:37888
	ds_read_b128 v[104:107], v90 offset:38912
	ds_read_b128 v[88:91], v90 offset:39936
	ds_read_b128 v[108:111], v78
	ds_read_b128 v[112:115], v78 offset:1024
	ds_read_b128 v[116:119], v78 offset:2048
	ds_read_b128 v[120:123], v78 offset:3072
	ds_read_b128 v[124:127], v78 offset:4096
	ds_read_b128 v[128:131], v78 offset:5120
	ds_read_b128 v[132:135], v78 offset:6144
	ds_read_b128 v[136:139], v78 offset:7168
	s_waitcnt vmcnt(0)
	s_waitcnt lgkmcnt(0)
	s_barrier
	s_setprio 1
	s_waitcnt lgkmcnt(0)
	v_mfma_f32_16x16x32_f16 v[62:65], v[66:69], v[108:111], v[62:65]
	v_mfma_f32_16x16x32_f16 v[58:61], v[84:87], v[108:111], v[58:61]
	v_mfma_f32_16x16x32_f16 v[54:57], v[96:99], v[108:111], v[54:57]
	v_mfma_f32_16x16x32_f16 v[50:53], v[104:107], v[108:111], v[50:53]
	v_mfma_f32_16x16x32_f16 v[46:49], v[66:69], v[116:119], v[46:49]
	v_mfma_f32_16x16x32_f16 v[42:45], v[84:87], v[116:119], v[42:45]
	v_mfma_f32_16x16x32_f16 v[38:41], v[96:99], v[116:119], v[38:41]
	v_mfma_f32_16x16x32_f16 v[34:37], v[104:107], v[116:119], v[34:37]
	v_mfma_f32_16x16x32_f16 v[30:33], v[66:69], v[124:127], v[30:33]
	v_mfma_f32_16x16x32_f16 v[26:29], v[84:87], v[124:127], v[26:29]
	v_mfma_f32_16x16x32_f16 v[22:25], v[96:99], v[124:127], v[22:25]
	v_mfma_f32_16x16x32_f16 v[18:21], v[104:107], v[124:127], v[18:21]
	v_mfma_f32_16x16x32_f16 v[14:17], v[66:69], v[132:135], v[14:17]
	v_mfma_f32_16x16x32_f16 v[10:13], v[84:87], v[132:135], v[10:13]
	v_mfma_f32_16x16x32_f16 v[6:9], v[96:99], v[132:135], v[6:9]
	v_mfma_f32_16x16x32_f16 v[2:5], v[104:107], v[132:135], v[2:5]
	v_mfma_f32_16x16x32_f16 v[62:65], v[70:73], v[112:115], v[62:65]
	v_mfma_f32_16x16x32_f16 v[58:61], v[92:95], v[112:115], v[58:61]
	v_mfma_f32_16x16x32_f16 v[54:57], v[100:103], v[112:115], v[54:57]
	v_mfma_f32_16x16x32_f16 v[50:53], v[88:91], v[112:115], v[50:53]
	v_mfma_f32_16x16x32_f16 v[46:49], v[70:73], v[120:123], v[46:49]
	v_mfma_f32_16x16x32_f16 v[42:45], v[92:95], v[120:123], v[42:45]
	v_mfma_f32_16x16x32_f16 v[38:41], v[100:103], v[120:123], v[38:41]
	v_mfma_f32_16x16x32_f16 v[34:37], v[88:91], v[120:123], v[34:37]
	v_mfma_f32_16x16x32_f16 v[30:33], v[70:73], v[128:131], v[30:33]
	v_mfma_f32_16x16x32_f16 v[26:29], v[92:95], v[128:131], v[26:29]
	v_mfma_f32_16x16x32_f16 v[22:25], v[100:103], v[128:131], v[22:25]
	v_mfma_f32_16x16x32_f16 v[18:21], v[88:91], v[128:131], v[18:21]
	v_mfma_f32_16x16x32_f16 v[14:17], v[70:73], v[136:139], v[14:17]
	v_mfma_f32_16x16x32_f16 v[10:13], v[92:95], v[136:139], v[10:13]
	v_mfma_f32_16x16x32_f16 v[6:9], v[100:103], v[136:139], v[6:9]
	v_mfma_f32_16x16x32_f16 v[2:5], v[88:91], v[136:139], v[2:5]
	s_setprio 0
	s_barrier
	ds_read_b128 v[66:69], v83
	ds_read_b128 v[70:73], v83 offset:1024
	ds_read_b128 v[84:87], v83 offset:2048
	ds_read_b128 v[88:91], v83 offset:3072
	ds_read_b128 v[92:95], v83 offset:4096
	ds_read_b128 v[96:99], v83 offset:5120
	ds_read_b128 v[100:103], v83 offset:6144
	ds_read_b128 v[80:83], v83 offset:7168
	ds_read_b128 v[104:107], v78 offset:49152
	ds_read_b128 v[108:111], v78 offset:50176
	ds_read_b128 v[112:115], v78 offset:51200
	ds_read_b128 v[116:119], v78 offset:52224
	ds_read_b128 v[120:123], v78 offset:53248
	ds_read_b128 v[124:127], v78 offset:54272
	ds_read_b128 v[128:131], v78 offset:55296
	ds_read_b128 v[76:79], v78 offset:56320
	s_waitcnt lgkmcnt(0)
	s_barrier
	s_setprio 1
	s_waitcnt lgkmcnt(0)
	v_mfma_f32_16x16x32_f16 v[62:65], v[66:69], v[104:107], v[62:65]
	v_mfma_f32_16x16x32_f16 v[58:61], v[84:87], v[104:107], v[58:61]
	v_mfma_f32_16x16x32_f16 v[54:57], v[92:95], v[104:107], v[54:57]
	v_mfma_f32_16x16x32_f16 v[50:53], v[100:103], v[104:107], v[50:53]
	v_mfma_f32_16x16x32_f16 v[46:49], v[66:69], v[112:115], v[46:49]
	v_mfma_f32_16x16x32_f16 v[42:45], v[84:87], v[112:115], v[42:45]
	v_mfma_f32_16x16x32_f16 v[38:41], v[92:95], v[112:115], v[38:41]
	v_mfma_f32_16x16x32_f16 v[34:37], v[100:103], v[112:115], v[34:37]
	v_mfma_f32_16x16x32_f16 v[30:33], v[66:69], v[120:123], v[30:33]
	v_mfma_f32_16x16x32_f16 v[26:29], v[84:87], v[120:123], v[26:29]
	v_mfma_f32_16x16x32_f16 v[22:25], v[92:95], v[120:123], v[22:25]
	v_mfma_f32_16x16x32_f16 v[18:21], v[100:103], v[120:123], v[18:21]
	v_mfma_f32_16x16x32_f16 v[14:17], v[66:69], v[128:131], v[14:17]
	v_mfma_f32_16x16x32_f16 v[10:13], v[84:87], v[128:131], v[10:13]
	v_mfma_f32_16x16x32_f16 v[6:9], v[92:95], v[128:131], v[6:9]
	v_mfma_f32_16x16x32_f16 v[2:5], v[100:103], v[128:131], v[2:5]
	v_mfma_f32_16x16x32_f16 v[62:65], v[70:73], v[108:111], v[62:65]
	v_mfma_f32_16x16x32_f16 v[58:61], v[88:91], v[108:111], v[58:61]
	v_mfma_f32_16x16x32_f16 v[54:57], v[96:99], v[108:111], v[54:57]
	v_mfma_f32_16x16x32_f16 v[50:53], v[80:83], v[108:111], v[50:53]
	v_mfma_f32_16x16x32_f16 v[46:49], v[70:73], v[116:119], v[46:49]
	v_mfma_f32_16x16x32_f16 v[42:45], v[88:91], v[116:119], v[42:45]
	v_mfma_f32_16x16x32_f16 v[38:41], v[96:99], v[116:119], v[38:41]
	v_mfma_f32_16x16x32_f16 v[34:37], v[80:83], v[116:119], v[34:37]
	v_mfma_f32_16x16x32_f16 v[30:33], v[70:73], v[124:127], v[30:33]
	v_mfma_f32_16x16x32_f16 v[26:29], v[88:91], v[124:127], v[26:29]
	v_mfma_f32_16x16x32_f16 v[22:25], v[96:99], v[124:127], v[22:25]
	v_mfma_f32_16x16x32_f16 v[18:21], v[80:83], v[124:127], v[18:21]
	v_mfma_f32_16x16x32_f16 v[14:17], v[70:73], v[76:79], v[14:17]
	v_mfma_f32_16x16x32_f16 v[10:13], v[88:91], v[76:79], v[10:13]
	v_mfma_f32_16x16x32_f16 v[6:9], v[96:99], v[76:79], v[6:9]
	v_mfma_f32_16x16x32_f16 v[2:5], v[80:83], v[76:79], v[2:5]
	s_setprio 0
	s_barrier
	s_and_saveexec_b64 s[4:5], s[0:1]
	s_cbranch_execz .LBB1_116
	s_barrier

	.amdhsa_kernel _Z8gemm_qkvPKDF16_S0_PKfS2_S2_PDF16_S3_S3_
		.amdhsa_group_segment_fixed_size 0
		.amdhsa_private_segment_fixed_size 0
		.amdhsa_kernarg_size 64
		.amdhsa_user_sgpr_count 2
		.amdhsa_user_sgpr_dispatch_ptr 0
		.amdhsa_user_sgpr_queue_ptr 0
		.amdhsa_user_sgpr_kernarg_segment_ptr 1
		.amdhsa_user_sgpr_dispatch_id 0
		.amdhsa_user_sgpr_kernarg_preload_length 0
		.amdhsa_user_sgpr_kernarg_preload_offset 0
		.amdhsa_user_sgpr_private_segment_size 0
		.amdhsa_uses_dynamic_stack 0
		.amdhsa_enable_private_segment 0
		.amdhsa_system_sgpr_workgroup_id_x 1
		.amdhsa_system_sgpr_workgroup_id_y 0
		.amdhsa_system_sgpr_workgroup_id_z 0
		.amdhsa_system_sgpr_workgroup_info 0
		.amdhsa_system_vgpr_workitem_id 0
		.amdhsa_next_free_vgpr 256
		.amdhsa_next_free_sgpr 92
		.amdhsa_accum_offset 256
		.amdhsa_reserve_vcc 1
		.amdhsa_float_round_mode_32 0
		.amdhsa_float_round_mode_16_64 0
		.amdhsa_float_denorm_mode_32 3
		.amdhsa_float_denorm_mode_16_64 3
		.amdhsa_dx10_clamp 1
		.amdhsa_ieee_mode 1
		.amdhsa_fp16_overflow 0
		.amdhsa_tg_split 0
		.amdhsa_exception_fp_ieee_invalid_op 0
		.amdhsa_exception_fp_denorm_src 0
		.amdhsa_exception_fp_ieee_div_zero 0
		.amdhsa_exception_fp_ieee_overflow 0
		.amdhsa_exception_fp_ieee_underflow 0
		.amdhsa_exception_fp_ieee_inexact 0
		.amdhsa_exception_int_div_zero 0
	.end_amdhsa_kernel

.LBB2_6:
	s_or_b64 exec, exec, s[16:17]
	v_lshlrev_b32_e32 v7, 6, v0
	v_lshlrev_b32_e32 v10, 2, v0
	v_and_b32_e32 v1, 48, v0
	v_and_b32_e32 v9, 0x3c0, v7
	v_and_b32_e32 v10, 32, v10
	v_bitop3_b32 v9, v9, v10, v1 bitop3:0x36
	v_add_u32_e32 v10, 0, v9
	v_and_b32_e32 v11, 0x4000, v7
	s_add_i32 s16, 0, 0x20000
	v_lshrrev_b32_e32 v76, 7, v0
	v_and_b32_e32 v12, 0x2000, v7
	v_add_u32_e32 v7, v10, v11
	v_add_u32_e32 v11, s9, v9
	v_add_u32_e32 v66, v4, v5
	v_lshlrev_b32_e32 v4, 5, v6
	v_lshlrev_b32_e32 v3, 12, v3
	s_mov_b32 s9, 0x70000
	s_add_u32 s4, s4, s14
	v_add_u32_e32 v13, 0x18000, v7
	v_add_u32_e32 v83, v7, v12
	v_and_or_b32 v4, v4, s9, v3
	v_mov_b32_e32 v5, v67
	s_addc_u32 s5, s5, s15
	v_lshl_or_b32 v6, v76, 16, v3
	v_mov_b32_e32 v7, v67
	v_lshl_add_u64 v[68:69], s[4:5], 0, v[4:5]
	v_lshl_add_u64 v[70:71], s[4:5], 0, v[6:7]
	s_add_u32 s4, s6, s12
	v_bfe_u32 v77, v0, 6, 1
	s_waitcnt vmcnt(6)
	s_addc_u32 s5, s7, s13
	s_add_i32 s6, 0, 0x18000
	s_add_i32 s12, 0, 0x1c000
	v_lshlrev_b32_e32 v8, 13, v77
	v_add_u32_e32 v9, s16, v9
	v_add_u32_e32 v91, s16, v2
	v_add_u32_e32 v92, s6, v2
	v_add_u32_e32 v93, s12, v2
	v_lshl_add_u64 v[72:73], s[4:5], 0, v[4:5]
	v_lshl_add_u64 v[74:75], s[4:5], 0, v[6:7]
	s_mov_b32 s9, -3
	v_add_u32_e32 v90, v10, v8
	s_mov_b64 s[4:5], 0x100
	s_mov_b64 s[6:7], 0x80100
	v_add_u32_e32 v89, v11, v8
	s_mov_b64 s[12:13], 0x180
	s_mov_b64 s[14:15], 0x80180
	v_add_u32_e32 v94, v9, v8
	v_add_u32_e32 v95, v13, v12
	s_mov_b64 s[16:17], 0x200
	s_mov_b64 s[18:19], 0x80200
	v_mov_b32_e32 v2, v67
	v_mov_b32_e32 v3, v67
	v_mov_b32_e32 v4, v67
	v_mov_b32_e32 v6, v67
	v_mov_b32_e32 v8, v67
	v_mov_b32_e32 v9, v67
	v_mov_b32_e32 v10, v67
	v_mov_b32_e32 v11, v67
	v_mov_b32_e32 v12, v67
	v_mov_b32_e32 v13, v67
	v_mov_b32_e32 v14, v67
	v_mov_b32_e32 v15, v67
	v_mov_b32_e32 v16, v67
	v_mov_b32_e32 v17, v67
	v_mov_b32_e32 v18, v67
	v_mov_b32_e32 v19, v67
	v_mov_b32_e32 v20, v67
	v_mov_b32_e32 v21, v67
	v_mov_b32_e32 v22, v67
	v_mov_b32_e32 v23, v67
	v_mov_b32_e32 v24, v67
	v_mov_b32_e32 v25, v67
	v_mov_b32_e32 v26, v67
	v_mov_b32_e32 v27, v67
	v_mov_b32_e32 v28, v67
	v_mov_b32_e32 v29, v67
	v_mov_b32_e32 v30, v67
	v_mov_b32_e32 v31, v67
	v_mov_b32_e32 v32, v67
	v_mov_b32_e32 v33, v67
	v_mov_b32_e32 v34, v67
	v_mov_b32_e32 v35, v67
	v_mov_b32_e32 v36, v67
	v_mov_b32_e32 v37, v67
	v_mov_b32_e32 v38, v67
	v_mov_b32_e32 v39, v67
	v_mov_b32_e32 v40, v67
	v_mov_b32_e32 v41, v67
	v_mov_b32_e32 v42, v67
	v_mov_b32_e32 v43, v67
	v_mov_b32_e32 v44, v67
	v_mov_b32_e32 v45, v67
	v_mov_b32_e32 v46, v67
	v_mov_b32_e32 v47, v67
	v_mov_b32_e32 v48, v67
	v_mov_b32_e32 v49, v67
	v_mov_b32_e32 v50, v67
	v_mov_b32_e32 v51, v67
	v_mov_b32_e32 v52, v67
	v_mov_b32_e32 v53, v67
	v_mov_b32_e32 v54, v67
	v_mov_b32_e32 v55, v67
	v_mov_b32_e32 v56, v67
	v_mov_b32_e32 v57, v67
	v_mov_b32_e32 v58, v67
	v_mov_b32_e32 v59, v67
	v_mov_b32_e32 v60, v67
	v_mov_b32_e32 v61, v67
	v_mov_b32_e32 v62, v67
	v_mov_b32_e32 v63, v67
	v_mov_b32_e32 v64, v67
	v_mov_b32_e32 v65, v67
	v_add_u32_e32 v96, 0x19000, v83
	v_add_u32_e32 v97, 0x19400, v83
	v_add_u32_e32 v98, 0x19800, v83
	v_add_u32_e32 v99, 0x19c00, v83
	v_add_u32_e32 v100, 0x2000, v91
	v_add_u32_e32 v101, 0x2000, v92
	v_add_u32_e32 v102, 0x2000, v93
	v_add_u32_e32 v103, 0x2000, v85
	v_add_u32_e32 v104, 0x2000, v88
	s_barrier
	s_barrier
	s_nop 1
	v_readfirstlane_b32 s50, v91
	v_readfirstlane_b32 s51, v100
	v_readfirstlane_b32 s52, v92
	v_readfirstlane_b32 s53, v101
	v_readfirstlane_b32 s54, v93
	v_readfirstlane_b32 s55, v102
	v_readfirstlane_b32 s56, v79
	v_readfirstlane_b32 s57, v80
	v_readfirstlane_b32 s58, v78
	v_readfirstlane_b32 s59, v81
	v_readfirstlane_b32 s60, v82
	v_readfirstlane_b32 s61, v84
	v_readfirstlane_b32 s62, v85
	v_readfirstlane_b32 s63, v103
	v_readfirstlane_b32 s64, v86
	v_readfirstlane_b32 s65, v87
	v_readfirstlane_b32 s66, v88
	v_readfirstlane_b32 s67, v104
.LBB2_7:
	v_lshl_add_u64 v[170:171], v[74:75], 0, v[66:67]
	v_lshl_add_u64 v[106:107], v[170:171], 0, s[4:5]
	s_mov_b32 m0, s50
	v_lshl_add_u64 v[172:173], v[72:73], 0, v[66:67]
	global_load_lds_dwordx4 v[106:107], off
	v_lshl_add_u64 v[106:107], v[172:173], 0, s[4:5]
	s_mov_b32 m0, s51
	v_lshl_add_u64 v[174:175], v[70:71], 0, v[66:67]
	global_load_lds_dwordx4 v[106:107], off
	v_lshl_add_u64 v[106:107], v[174:175], 0, s[4:5]
	s_mov_b32 m0, s52
	v_lshl_add_u64 v[176:177], v[68:69], 0, v[66:67]
	global_load_lds_dwordx4 v[106:107], off
	v_lshl_add_u64 v[106:107], v[176:177], 0, s[4:5]
	s_mov_b32 m0, s53
	s_nop 0
	global_load_lds_dwordx4 v[106:107], off
	v_lshl_add_u64 v[106:107], v[174:175], 0, s[6:7]
	s_mov_b32 m0, s54
	s_nop 0
	global_load_lds_dwordx4 v[106:107], off
	v_lshl_add_u64 v[106:107], v[176:177], 0, s[6:7]
	s_mov_b32 m0, s55
	s_nop 0
	global_load_lds_dwordx4 v[106:107], off
	ds_read_b128 v[106:109], v90 offset:32768
	ds_read_b128 v[110:113], v90 offset:33792
	ds_read_b128 v[114:117], v90 offset:34816
	ds_read_b128 v[118:121], v90 offset:35840
	ds_read_b128 v[122:125], v90 offset:36864
	ds_read_b128 v[126:129], v90 offset:37888
	ds_read_b128 v[130:133], v90 offset:38912
	ds_read_b128 v[134:137], v90 offset:39936
	ds_read_b128 v[138:141], v83
	ds_read_b128 v[142:145], v83 offset:1024
	ds_read_b128 v[146:149], v83 offset:2048
	ds_read_b128 v[150:153], v83 offset:3072
	ds_read_b128 v[154:157], v83 offset:4096
	ds_read_b128 v[158:161], v83 offset:5120
	ds_read_b128 v[162:165], v83 offset:6144
	ds_read_b128 v[166:169], v83 offset:7168
	s_waitcnt vmcnt(6)
	s_waitcnt lgkmcnt(0)
	s_barrier
	s_setprio 1
	s_waitcnt lgkmcnt(0)
	v_mfma_f32_16x16x32_f16 v[62:65], v[106:109], v[138:141], v[62:65]
	v_mfma_f32_16x16x32_f16 v[58:61], v[114:117], v[138:141], v[58:61]
	v_mfma_f32_16x16x32_f16 v[54:57], v[122:125], v[138:141], v[54:57]
	v_mfma_f32_16x16x32_f16 v[50:53], v[130:133], v[138:141], v[50:53]
	v_mfma_f32_16x16x32_f16 v[46:49], v[106:109], v[146:149], v[46:49]
	v_mfma_f32_16x16x32_f16 v[42:45], v[114:117], v[146:149], v[42:45]
	v_mfma_f32_16x16x32_f16 v[38:41], v[122:125], v[146:149], v[38:41]
	v_mfma_f32_16x16x32_f16 v[34:37], v[130:133], v[146:149], v[34:37]
	v_mfma_f32_16x16x32_f16 v[30:33], v[106:109], v[154:157], v[30:33]
	v_mfma_f32_16x16x32_f16 v[26:29], v[114:117], v[154:157], v[26:29]
	v_mfma_f32_16x16x32_f16 v[22:25], v[122:125], v[154:157], v[22:25]
	v_mfma_f32_16x16x32_f16 v[18:21], v[130:133], v[154:157], v[18:21]
	v_mfma_f32_16x16x32_f16 v[14:17], v[106:109], v[162:165], v[14:17]
	v_mfma_f32_16x16x32_f16 v[10:13], v[114:117], v[162:165], v[10:13]
	v_mfma_f32_16x16x32_f16 v[6:9], v[122:125], v[162:165], v[6:9]
	v_mfma_f32_16x16x32_f16 v[2:5], v[130:133], v[162:165], v[2:5]
	v_mfma_f32_16x16x32_f16 v[62:65], v[110:113], v[142:145], v[62:65]
	v_mfma_f32_16x16x32_f16 v[58:61], v[118:121], v[142:145], v[58:61]
	v_mfma_f32_16x16x32_f16 v[54:57], v[126:129], v[142:145], v[54:57]
	v_mfma_f32_16x16x32_f16 v[50:53], v[134:137], v[142:145], v[50:53]
	v_mfma_f32_16x16x32_f16 v[46:49], v[110:113], v[150:153], v[46:49]
	v_mfma_f32_16x16x32_f16 v[42:45], v[118:121], v[150:153], v[42:45]
	v_mfma_f32_16x16x32_f16 v[38:41], v[126:129], v[150:153], v[38:41]
	v_mfma_f32_16x16x32_f16 v[34:37], v[134:137], v[150:153], v[34:37]
	v_mfma_f32_16x16x32_f16 v[30:33], v[110:113], v[158:161], v[30:33]
	v_mfma_f32_16x16x32_f16 v[26:29], v[118:121], v[158:161], v[26:29]
	v_mfma_f32_16x16x32_f16 v[22:25], v[126:129], v[158:161], v[22:25]
	v_mfma_f32_16x16x32_f16 v[18:21], v[134:137], v[158:161], v[18:21]
	v_mfma_f32_16x16x32_f16 v[14:17], v[110:113], v[166:169], v[14:17]
	v_mfma_f32_16x16x32_f16 v[10:13], v[118:121], v[166:169], v[10:13]
	v_mfma_f32_16x16x32_f16 v[6:9], v[126:129], v[166:169], v[6:9]
	v_mfma_f32_16x16x32_f16 v[2:5], v[134:137], v[166:169], v[2:5]
	s_setprio 0
	s_barrier
	v_lshl_add_u64 v[138:139], v[170:171], 0, s[12:13]
	s_mov_b32 m0, s56
	ds_read_b128 v[106:109], v83 offset:49152
	ds_read_b128 v[110:113], v83 offset:50176
	ds_read_b128 v[114:117], v83 offset:51200
	ds_read_b128 v[118:121], v83 offset:52224
	ds_read_b128 v[122:125], v83 offset:53248
	ds_read_b128 v[126:129], v83 offset:54272
	ds_read_b128 v[130:133], v83 offset:55296
	ds_read_b128 v[134:137], v83 offset:56320
	global_load_lds_dwordx4 v[138:139], off
	v_lshl_add_u64 v[138:139], v[172:173], 0, s[12:13]
	s_mov_b32 m0, s57
	s_nop 0
	global_load_lds_dwordx4 v[138:139], off
	v_lshl_add_u64 v[138:139], v[174:175], 0, s[12:13]
	s_mov_b32 m0, s58
	s_nop 0
	global_load_lds_dwordx4 v[138:139], off
	v_lshl_add_u64 v[138:139], v[176:177], 0, s[12:13]
	s_mov_b32 m0, s59
	s_nop 0
	global_load_lds_dwordx4 v[138:139], off
	v_lshl_add_u64 v[138:139], v[174:175], 0, s[14:15]
	s_mov_b32 m0, s60
	s_nop 0
	global_load_lds_dwordx4 v[138:139], off
	v_lshl_add_u64 v[138:139], v[176:177], 0, s[14:15]
	s_mov_b32 m0, s61
	s_nop 0
	global_load_lds_dwordx4 v[138:139], off
	ds_read_b128 v[138:141], v89
	ds_read_b128 v[142:145], v89 offset:1024
	ds_read_b128 v[146:149], v89 offset:2048
	ds_read_b128 v[150:153], v89 offset:3072
	ds_read_b128 v[154:157], v89 offset:4096
	ds_read_b128 v[158:161], v89 offset:5120
	ds_read_b128 v[162:165], v89 offset:6144
	ds_read_b128 v[166:169], v89 offset:7168
	s_waitcnt vmcnt(6)
	s_waitcnt lgkmcnt(0)
	s_barrier
	s_setprio 1
	s_waitcnt lgkmcnt(0)
	v_mfma_f32_16x16x32_f16 v[62:65], v[138:141], v[106:109], v[62:65]
	v_mfma_f32_16x16x32_f16 v[58:61], v[146:149], v[106:109], v[58:61]
	v_mfma_f32_16x16x32_f16 v[54:57], v[154:157], v[106:109], v[54:57]
	v_mfma_f32_16x16x32_f16 v[50:53], v[162:165], v[106:109], v[50:53]
	v_mfma_f32_16x16x32_f16 v[46:49], v[138:141], v[114:117], v[46:49]
	v_mfma_f32_16x16x32_f16 v[42:45], v[146:149], v[114:117], v[42:45]
	v_mfma_f32_16x16x32_f16 v[38:41], v[154:157], v[114:117], v[38:41]
	v_mfma_f32_16x16x32_f16 v[34:37], v[162:165], v[114:117], v[34:37]
	v_mfma_f32_16x16x32_f16 v[30:33], v[138:141], v[122:125], v[30:33]
	v_mfma_f32_16x16x32_f16 v[26:29], v[146:149], v[122:125], v[26:29]
	v_mfma_f32_16x16x32_f16 v[22:25], v[154:157], v[122:125], v[22:25]
	v_mfma_f32_16x16x32_f16 v[18:21], v[162:165], v[122:125], v[18:21]
	v_mfma_f32_16x16x32_f16 v[14:17], v[138:141], v[130:133], v[14:17]
	v_mfma_f32_16x16x32_f16 v[10:13], v[146:149], v[130:133], v[10:13]
	v_mfma_f32_16x16x32_f16 v[6:9], v[154:157], v[130:133], v[6:9]
	v_mfma_f32_16x16x32_f16 v[2:5], v[162:165], v[130:133], v[2:5]
	v_mfma_f32_16x16x32_f16 v[62:65], v[142:145], v[110:113], v[62:65]
	v_mfma_f32_16x16x32_f16 v[58:61], v[150:153], v[110:113], v[58:61]
	v_mfma_f32_16x16x32_f16 v[54:57], v[158:161], v[110:113], v[54:57]
	v_mfma_f32_16x16x32_f16 v[50:53], v[166:169], v[110:113], v[50:53]
	v_mfma_f32_16x16x32_f16 v[46:49], v[142:145], v[118:121], v[46:49]
	v_mfma_f32_16x16x32_f16 v[42:45], v[150:153], v[118:121], v[42:45]
	v_mfma_f32_16x16x32_f16 v[38:41], v[158:161], v[118:121], v[38:41]
	v_mfma_f32_16x16x32_f16 v[34:37], v[166:169], v[118:121], v[34:37]
	v_mfma_f32_16x16x32_f16 v[30:33], v[142:145], v[126:129], v[30:33]
	v_mfma_f32_16x16x32_f16 v[26:29], v[150:153], v[126:129], v[26:29]
	v_mfma_f32_16x16x32_f16 v[22:25], v[158:161], v[126:129], v[22:25]
	v_mfma_f32_16x16x32_f16 v[18:21], v[166:169], v[126:129], v[18:21]
	v_mfma_f32_16x16x32_f16 v[14:17], v[142:145], v[134:137], v[14:17]
	v_mfma_f32_16x16x32_f16 v[10:13], v[150:153], v[134:137], v[10:13]
	v_mfma_f32_16x16x32_f16 v[6:9], v[158:161], v[134:137], v[6:9]
	v_mfma_f32_16x16x32_f16 v[2:5], v[166:169], v[134:137], v[2:5]
	s_setprio 0
	s_barrier
	v_lshl_add_u64 v[138:139], v[170:171], 0, s[16:17]
	s_mov_b32 m0, s62
	ds_read_b128 v[106:109], v95
	ds_read_b128 v[110:113], v95 offset:1024
	ds_read_b128 v[114:117], v95 offset:2048
	ds_read_b128 v[118:121], v95 offset:3072
	ds_read_b128 v[122:125], v96
	ds_read_b128 v[126:129], v97
	ds_read_b128 v[130:133], v98
	ds_read_b128 v[134:137], v99
	global_load_lds_dwordx4 v[138:139], off
	v_lshl_add_u64 v[138:139], v[172:173], 0, s[16:17]
	s_mov_b32 m0, s63
	s_nop 0
	global_load_lds_dwordx4 v[138:139], off
	v_lshl_add_u64 v[138:139], v[174:175], 0, s[16:17]
	s_mov_b32 m0, s64
	s_nop 0
	global_load_lds_dwordx4 v[138:139], off
	v_lshl_add_u64 v[138:139], v[176:177], 0, s[16:17]
	s_mov_b32 m0, s65
	s_nop 0
	global_load_lds_dwordx4 v[138:139], off
	v_lshl_add_u64 v[138:139], v[174:175], 0, s[18:19]
	s_mov_b32 m0, s66
	s_nop 0
	global_load_lds_dwordx4 v[138:139], off
	v_lshl_add_u64 v[138:139], v[176:177], 0, s[18:19]
	s_mov_b32 m0, s67
	s_nop 0
	global_load_lds_dwordx4 v[138:139], off
	ds_read_b128 v[138:141], v94
	ds_read_b128 v[142:145], v94 offset:1024
	ds_read_b128 v[146:149], v94 offset:2048
	ds_read_b128 v[150:153], v94 offset:3072
	ds_read_b128 v[154:157], v94 offset:4096
	ds_read_b128 v[158:161], v94 offset:5120
	ds_read_b128 v[162:165], v94 offset:6144
	ds_read_b128 v[166:169], v94 offset:7168
	s_waitcnt vmcnt(6)
	s_waitcnt lgkmcnt(0)
	s_barrier
	s_setprio 1
	s_waitcnt lgkmcnt(0)
	v_mfma_f32_16x16x32_f16 v[62:65], v[138:141], v[106:109], v[62:65]
	v_mfma_f32_16x16x32_f16 v[58:61], v[146:149], v[106:109], v[58:61]
	v_mfma_f32_16x16x32_f16 v[54:57], v[154:157], v[106:109], v[54:57]
	v_mfma_f32_16x16x32_f16 v[50:53], v[162:165], v[106:109], v[50:53]
	v_mfma_f32_16x16x32_f16 v[46:49], v[138:141], v[114:117], v[46:49]
	v_mfma_f32_16x16x32_f16 v[42:45], v[146:149], v[114:117], v[42:45]
	v_mfma_f32_16x16x32_f16 v[38:41], v[154:157], v[114:117], v[38:41]
	v_mfma_f32_16x16x32_f16 v[34:37], v[162:165], v[114:117], v[34:37]
	v_mfma_f32_16x16x32_f16 v[30:33], v[138:141], v[122:125], v[30:33]
	v_mfma_f32_16x16x32_f16 v[26:29], v[146:149], v[122:125], v[26:29]
	v_mfma_f32_16x16x32_f16 v[22:25], v[154:157], v[122:125], v[22:25]
	v_mfma_f32_16x16x32_f16 v[18:21], v[162:165], v[122:125], v[18:21]
	v_mfma_f32_16x16x32_f16 v[14:17], v[138:141], v[130:133], v[14:17]
	v_mfma_f32_16x16x32_f16 v[10:13], v[146:149], v[130:133], v[10:13]
	v_mfma_f32_16x16x32_f16 v[6:9], v[154:157], v[130:133], v[6:9]
	v_mfma_f32_16x16x32_f16 v[2:5], v[162:165], v[130:133], v[2:5]
	v_mfma_f32_16x16x32_f16 v[62:65], v[142:145], v[110:113], v[62:65]
	v_mfma_f32_16x16x32_f16 v[58:61], v[150:153], v[110:113], v[58:61]
	v_mfma_f32_16x16x32_f16 v[54:57], v[158:161], v[110:113], v[54:57]
	v_mfma_f32_16x16x32_f16 v[50:53], v[166:169], v[110:113], v[50:53]
	v_mfma_f32_16x16x32_f16 v[46:49], v[142:145], v[118:121], v[46:49]
	v_mfma_f32_16x16x32_f16 v[42:45], v[150:153], v[118:121], v[42:45]
	v_mfma_f32_16x16x32_f16 v[38:41], v[158:161], v[118:121], v[38:41]
	v_mfma_f32_16x16x32_f16 v[34:37], v[166:169], v[118:121], v[34:37]
	v_mfma_f32_16x16x32_f16 v[30:33], v[142:145], v[126:129], v[30:33]
	v_mfma_f32_16x16x32_f16 v[26:29], v[150:153], v[126:129], v[26:29]
	v_mfma_f32_16x16x32_f16 v[22:25], v[158:161], v[126:129], v[22:25]
	v_mfma_f32_16x16x32_f16 v[18:21], v[166:169], v[126:129], v[18:21]
	v_mfma_f32_16x16x32_f16 v[14:17], v[142:145], v[134:137], v[14:17]
	v_mfma_f32_16x16x32_f16 v[10:13], v[150:153], v[134:137], v[10:13]
	v_mfma_f32_16x16x32_f16 v[6:9], v[158:161], v[134:137], v[6:9]
	v_mfma_f32_16x16x32_f16 v[2:5], v[166:169], v[134:137], v[2:5]
	s_setprio 0
	s_barrier
	s_add_i32 s9, s9, 3
	v_lshl_add_u64 v[68:69], v[68:69], 0, s[12:13]
	v_lshl_add_u64 v[70:71], v[70:71], 0, s[12:13]
	v_lshl_add_u64 v[72:73], v[72:73], 0, s[12:13]
	s_cmp_lt_u32 s9, 27
	v_lshl_add_u64 v[74:75], v[74:75], 0, s[12:13]
	s_cbranch_scc1 .LBB2_7
	ds_read_b128 v[66:69], v90 offset:32768
	ds_read_b128 v[70:73], v90 offset:33792
	ds_read_b128 v[78:81], v90 offset:34816
	ds_read_b128 v[84:87], v90 offset:35840
	ds_read_b128 v[92:95], v90 offset:36864
	ds_read_b128 v[96:99], v90 offset:37888
	ds_read_b128 v[100:103], v90 offset:38912
	ds_read_b128 v[104:107], v90 offset:39936
	ds_read_b128 v[108:111], v83
	ds_read_b128 v[112:115], v83 offset:1024
	ds_read_b128 v[116:119], v83 offset:2048
	ds_read_b128 v[120:123], v83 offset:3072
	ds_read_b128 v[124:127], v83 offset:4096
	ds_read_b128 v[128:131], v83 offset:5120
	ds_read_b128 v[132:135], v83 offset:6144
	ds_read_b128 v[136:139], v83 offset:7168
	s_waitcnt vmcnt(0)
	s_waitcnt lgkmcnt(0)
	s_barrier
	s_setprio 1
	s_waitcnt lgkmcnt(0)
	v_mfma_f32_16x16x32_f16 v[62:65], v[66:69], v[108:111], v[62:65]
	v_mfma_f32_16x16x32_f16 v[58:61], v[78:81], v[108:111], v[58:61]
	v_mfma_f32_16x16x32_f16 v[54:57], v[92:95], v[108:111], v[54:57]
	v_mfma_f32_16x16x32_f16 v[50:53], v[100:103], v[108:111], v[50:53]
	v_mfma_f32_16x16x32_f16 v[46:49], v[66:69], v[116:119], v[46:49]
	v_mfma_f32_16x16x32_f16 v[42:45], v[78:81], v[116:119], v[42:45]
	v_mfma_f32_16x16x32_f16 v[38:41], v[92:95], v[116:119], v[38:41]
	v_mfma_f32_16x16x32_f16 v[34:37], v[100:103], v[116:119], v[34:37]
	v_mfma_f32_16x16x32_f16 v[62:65], v[70:73], v[112:115], v[62:65]
	v_mfma_f32_16x16x32_f16 v[58:61], v[84:87], v[112:115], v[58:61]
	v_mfma_f32_16x16x32_f16 v[54:57], v[96:99], v[112:115], v[54:57]
	v_mfma_f32_16x16x32_f16 v[50:53], v[104:107], v[112:115], v[50:53]
	v_mfma_f32_16x16x32_f16 v[46:49], v[70:73], v[120:123], v[46:49]
	v_mfma_f32_16x16x32_f16 v[42:45], v[84:87], v[120:123], v[42:45]
	v_mfma_f32_16x16x32_f16 v[38:41], v[96:99], v[120:123], v[38:41]
	v_mfma_f32_16x16x32_f16 v[34:37], v[104:107], v[120:123], v[34:37]
	v_mfma_f32_16x16x32_f16 v[30:33], v[66:69], v[124:127], v[30:33]
	v_mfma_f32_16x16x32_f16 v[26:29], v[78:81], v[124:127], v[26:29]
	v_mfma_f32_16x16x32_f16 v[22:25], v[92:95], v[124:127], v[22:25]
	v_mfma_f32_16x16x32_f16 v[18:21], v[100:103], v[124:127], v[18:21]
	v_mfma_f32_16x16x32_f16 v[14:17], v[66:69], v[132:135], v[14:17]
	v_mfma_f32_16x16x32_f16 v[10:13], v[78:81], v[132:135], v[10:13]
	v_mfma_f32_16x16x32_f16 v[6:9], v[92:95], v[132:135], v[6:9]
	v_mfma_f32_16x16x32_f16 v[2:5], v[100:103], v[132:135], v[2:5]
	v_mfma_f32_16x16x32_f16 v[108:111], v[70:73], v[128:131], v[30:33]
	v_mfma_f32_16x16x32_f16 v[112:115], v[84:87], v[128:131], v[26:29]
	v_mfma_f32_16x16x32_f16 v[116:119], v[96:99], v[128:131], v[22:25]
	v_mfma_f32_16x16x32_f16 v[120:123], v[104:107], v[128:131], v[18:21]
	v_mfma_f32_16x16x32_f16 v[66:69], v[70:73], v[136:139], v[14:17]
	v_mfma_f32_16x16x32_f16 v[70:73], v[84:87], v[136:139], v[10:13]
	v_mfma_f32_16x16x32_f16 v[78:81], v[96:99], v[136:139], v[6:9]
	v_mfma_f32_16x16x32_f16 v[84:87], v[104:107], v[136:139], v[2:5]
	s_setprio 0
	s_barrier
	ds_read_b128 v[90:93], v89
	ds_read_b128 v[94:97], v89 offset:1024
	ds_read_b128 v[98:101], v89 offset:2048
	ds_read_b128 v[102:105], v89 offset:3072
	ds_read_b128 v[124:127], v89 offset:4096
	ds_read_b128 v[128:131], v89 offset:5120
	ds_read_b128 v[132:135], v89 offset:6144
	ds_read_b128 v[136:139], v89 offset:7168
	ds_read_b128 v[14:17], v83 offset:49152
	ds_read_b128 v[18:21], v83 offset:50176
	ds_read_b128 v[30:33], v83 offset:51200
	ds_read_b128 v[140:143], v83 offset:52224
	ds_read_b128 v[144:147], v83 offset:53248
	ds_read_b128 v[148:151], v83 offset:54272
	ds_read_b128 v[152:155], v83 offset:55296
	ds_read_b128 v[156:159], v83 offset:56320
	s_waitcnt lgkmcnt(0)
	s_barrier
	s_setprio 1
	s_waitcnt lgkmcnt(0)
	v_mfma_f32_16x16x32_f16 v[2:5], v[90:93], v[14:17], v[62:65]
	v_mfma_f32_16x16x32_f16 v[6:9], v[98:101], v[14:17], v[58:61]
	v_mfma_f32_16x16x32_f16 v[10:13], v[124:127], v[14:17], v[54:57]
	v_mfma_f32_16x16x32_f16 v[14:17], v[132:135], v[14:17], v[50:53]
	v_mfma_f32_16x16x32_f16 v[2:5], v[94:97], v[18:21], v[2:5]
	v_mfma_f32_16x16x32_f16 v[6:9], v[102:105], v[18:21], v[6:9]
	v_mfma_f32_16x16x32_f16 v[10:13], v[128:131], v[18:21], v[10:13]
	v_mfma_f32_16x16x32_f16 v[14:17], v[136:139], v[18:21], v[14:17]
	v_mfma_f32_16x16x32_f16 v[18:21], v[90:93], v[30:33], v[46:49]
	v_mfma_f32_16x16x32_f16 v[22:25], v[98:101], v[30:33], v[42:45]
	v_mfma_f32_16x16x32_f16 v[26:29], v[124:127], v[30:33], v[38:41]
	v_mfma_f32_16x16x32_f16 v[30:33], v[132:135], v[30:33], v[34:37]
	v_mfma_f32_16x16x32_f16 v[34:37], v[90:93], v[144:147], v[108:111]
	v_mfma_f32_16x16x32_f16 v[38:41], v[98:101], v[144:147], v[112:115]
	v_mfma_f32_16x16x32_f16 v[42:45], v[124:127], v[144:147], v[116:119]
	v_mfma_f32_16x16x32_f16 v[46:49], v[132:135], v[144:147], v[120:123]
	v_mfma_f32_16x16x32_f16 v[50:53], v[90:93], v[152:155], v[66:69]
	v_mfma_f32_16x16x32_f16 v[54:57], v[98:101], v[152:155], v[70:73]
	v_mfma_f32_16x16x32_f16 v[58:61], v[124:127], v[152:155], v[78:81]
	v_mfma_f32_16x16x32_f16 v[62:65], v[132:135], v[152:155], v[84:87]
	v_mfma_f32_16x16x32_f16 v[18:21], v[94:97], v[140:143], v[18:21]
	v_mfma_f32_16x16x32_f16 v[22:25], v[102:105], v[140:143], v[22:25]
	v_mfma_f32_16x16x32_f16 v[26:29], v[128:131], v[140:143], v[26:29]
	v_mfma_f32_16x16x32_f16 v[30:33], v[136:139], v[140:143], v[30:33]
	v_mfma_f32_16x16x32_f16 v[34:37], v[94:97], v[148:151], v[34:37]
	v_mfma_f32_16x16x32_f16 v[38:41], v[102:105], v[148:151], v[38:41]
	v_mfma_f32_16x16x32_f16 v[42:45], v[128:131], v[148:151], v[42:45]
	v_mfma_f32_16x16x32_f16 v[46:49], v[136:139], v[148:151], v[46:49]
	v_mfma_f32_16x16x32_f16 v[50:53], v[94:97], v[156:159], v[50:53]
	v_mfma_f32_16x16x32_f16 v[54:57], v[102:105], v[156:159], v[54:57]
	v_mfma_f32_16x16x32_f16 v[58:61], v[128:131], v[156:159], v[58:61]
	v_mfma_f32_16x16x32_f16 v[62:65], v[136:139], v[156:159], v[62:65]
	s_setprio 0
	s_movk_i32 s4, 0x100
	v_cmp_gt_u32_e32 vcc, s4, v0
	s_barrier
	s_and_saveexec_b64 s[4:5], vcc
	s_cbranch_execz .LBB2_10
	s_barrier

	.amdhsa_kernel _Z9gemm_projPKDF16_S0_PKfPf
		.amdhsa_group_segment_fixed_size 0
		.amdhsa_private_segment_fixed_size 0
		.amdhsa_kernarg_size 32
		.amdhsa_user_sgpr_count 2
		.amdhsa_user_sgpr_dispatch_ptr 0
		.amdhsa_user_sgpr_queue_ptr 0
		.amdhsa_user_sgpr_kernarg_segment_ptr 1
		.amdhsa_user_sgpr_dispatch_id 0
		.amdhsa_user_sgpr_kernarg_preload_length 0
		.amdhsa_user_sgpr_kernarg_preload_offset 0
		.amdhsa_user_sgpr_private_segment_size 0
		.amdhsa_uses_dynamic_stack 0
		.amdhsa_enable_private_segment 0
		.amdhsa_system_sgpr_workgroup_id_x 1
		.amdhsa_system_sgpr_workgroup_id_y 0
		.amdhsa_system_sgpr_workgroup_id_z 0
		.amdhsa_system_sgpr_workgroup_info 0
		.amdhsa_system_vgpr_workitem_id 0
		.amdhsa_next_free_vgpr 184
		.amdhsa_next_free_sgpr 68
		.amdhsa_accum_offset 184
		.amdhsa_reserve_vcc 1
		.amdhsa_float_round_mode_32 0
		.amdhsa_float_round_mode_16_64 0
		.amdhsa_float_denorm_mode_32 3
		.amdhsa_float_denorm_mode_16_64 3
		.amdhsa_dx10_clamp 1
		.amdhsa_ieee_mode 1
		.amdhsa_fp16_overflow 0
		.amdhsa_tg_split 0
		.amdhsa_exception_fp_ieee_invalid_op 0
		.amdhsa_exception_fp_denorm_src 0
		.amdhsa_exception_fp_ieee_div_zero 0
		.amdhsa_exception_fp_ieee_overflow 0
		.amdhsa_exception_fp_ieee_underflow 0
		.amdhsa_exception_fp_ieee_inexact 0
		.amdhsa_exception_int_div_zero 0
	.end_amdhsa_kernel

amdhsa.kernels:
  - .agpr_count:     0
    .args:
      - .actual_access:  read_only
        .address_space:  global
        .offset:         0
        .size:           8
        .value_kind:     global_buffer
      - .actual_access:  write_only
        .address_space:  global
        .offset:         8
        .size:           8
        .value_kind:     global_buffer
      - .offset:         16
        .size:           8
        .value_kind:     by_value
      - .actual_access:  read_only
        .address_space:  global
        .offset:         24
        .size:           8
        .value_kind:     global_buffer
      - .actual_access:  write_only
        .address_space:  global
        .offset:         32
        .size:           8
        .value_kind:     global_buffer
      - .offset:         40
        .size:           8
        .value_kind:     by_value
      - .actual_access:  read_only
        .address_space:  global
        .offset:         48
        .size:           8
        .value_kind:     global_buffer
      - .actual_access:  write_only
        .address_space:  global
        .offset:         56
        .size:           8
        .value_kind:     global_buffer
      - .offset:         64
        .size:           8
        .value_kind:     by_value
      - .offset:         72
        .size:           4
        .value_kind:     hidden_block_count_x
      - .offset:         76
        .size:           4
        .value_kind:     hidden_block_count_y
      - .offset:         80
        .size:           4
        .value_kind:     hidden_block_count_z
      - .offset:         84
        .size:           2
        .value_kind:     hidden_group_size_x
      - .offset:         86
        .size:           2
        .value_kind:     hidden_group_size_y
      - .offset:         88
        .size:           2
        .value_kind:     hidden_group_size_z
      - .offset:         90
        .size:           2
        .value_kind:     hidden_remainder_x
      - .offset:         92
        .size:           2
        .value_kind:     hidden_remainder_y
      - .offset:         94
        .size:           2
        .value_kind:     hidden_remainder_z
      - .offset:         112
        .size:           8
        .value_kind:     hidden_global_offset_x
      - .offset:         120
        .size:           8
        .value_kind:     hidden_global_offset_y
      - .offset:         128
        .size:           8
        .value_kind:     hidden_global_offset_z
      - .offset:         136
        .size:           2
        .value_kind:     hidden_grid_dims
    .group_segment_fixed_size: 0
    .kernarg_segment_align: 8
    .kernarg_segment_size: 328
    .language:       OpenCL C
    .language_version:
      - 2
      - 0
    .max_flat_workgroup_size: 256
    .name:           _Z12cvt3_f32_f16PKfPDF16_lS0_S1_lS0_S1_l
    .private_segment_fixed_size: 0
    .sgpr_count:     34
    .sgpr_spill_count: 0
    .symbol:         _Z12cvt3_f32_f16PKfPDF16_lS0_S1_lS0_S1_l.kd
    .uniform_work_group_size: 1
    .uses_dynamic_stack: false
    .vgpr_count:     16
    .vgpr_spill_count: 0
    .wavefront_size: 64
  - .agpr_count:     0
    .args:
      - .address_space:  global
        .offset:         0
        .size:           8
        .value_kind:     global_buffer
      - .address_space:  global
        .offset:         8
        .size:           8
        .value_kind:     global_buffer
      - .actual_access:  read_only
        .address_space:  global
        .offset:         16
        .size:           8
        .value_kind:     global_buffer
      - .actual_access:  read_only
        .address_space:  global
        .offset:         24
        .size:           8
        .value_kind:     global_buffer
      - .actual_access:  read_only
        .address_space:  global
        .offset:         32
        .size:           8
        .value_kind:     global_buffer
      - .actual_access:  write_only
        .address_space:  global
        .offset:         40
        .size:           8
        .value_kind:     global_buffer
      - .actual_access:  write_only
        .address_space:  global
        .offset:         48
        .size:           8
        .value_kind:     global_buffer
      - .actual_access:  write_only
        .address_space:  global
        .offset:         56
        .size:           8
        .value_kind:     global_buffer
    .group_segment_fixed_size: 0
    .kernarg_segment_align: 8
    .kernarg_segment_size: 64
    .language:       OpenCL C
    .language_version:
      - 2
      - 0
    .max_flat_workgroup_size: 512
    .name:           _Z8gemm_qkvPKDF16_S0_PKfS2_S2_PDF16_S3_S3_
    .private_segment_fixed_size: 0
    .sgpr_count:     98
    .sgpr_spill_count: 0
    .symbol:         _Z8gemm_qkvPKDF16_S0_PKfS2_S2_PDF16_S3_S3_.kd
    .uniform_work_group_size: 1
    .uses_dynamic_stack: false
    .vgpr_count:     256
    .vgpr_spill_count: 0
    .wavefront_size: 64
  - .agpr_count:     0
    .args:
      - .address_space:  global
        .offset:         0
        .size:           8
        .value_kind:     global_buffer
      - .address_space:  global
        .offset:         8
        .size:           8
        .value_kind:     global_buffer
      - .actual_access:  read_only
        .address_space:  global
        .offset:         16
        .size:           8
        .value_kind:     global_buffer
      - .actual_access:  write_only
        .address_space:  global
        .offset:         24
        .size:           8
        .value_kind:     global_buffer
    .group_segment_fixed_size: 0
    .kernarg_segment_align: 8
    .kernarg_segment_size: 32
    .language:       OpenCL C
    .language_version:
      - 2
      - 0
    .max_flat_workgroup_size: 512
    .name:           _Z9gemm_projPKDF16_S0_PKfPf
    .private_segment_fixed_size: 0
    .sgpr_count:     74
    .sgpr_spill_count: 0
    .symbol:         _Z9gemm_projPKDF16_S0_PKfPf.kd
    .uniform_work_group_size: 1
    .uses_dynamic_stack: false
    .vgpr_count:     184
    .vgpr_spill_count: 0
    .wavefront_size: 64
  - .agpr_count:     256
    .args:
      - .address_space:  global
        .offset:         0
        .size:           8
        .value_kind:     global_buffer
      - .address_space:  global
        .offset:         8
        .size:           8
        .value_kind:     global_buffer
      - .address_space:  global
        .offset:         16
        .size:           8
        .value_kind:     global_buffer
      - .actual_access:  write_only
        .address_space:  global
        .offset:         24
        .size:           8
        .value_kind:     global_buffer
      - .offset:         32
        .size:           4
        .value_kind:     hidden_block_count_x
      - .offset:         36
        .size:           4
        .value_kind:     hidden_block_count_y
      - .offset:         40
        .size:           4
        .value_kind:     hidden_block_count_z
      - .offset:         44
        .size:           2
        .value_kind:     hidden_group_size_x
      - .offset:         46
        .size:           2
        .value_kind:     hidden_group_size_y
      - .offset:         48
        .size:           2
        .value_kind:     hidden_group_size_z
      - .offset:         50
        .size:           2
        .value_kind:     hidden_remainder_x
      - .offset:         52
        .size:           2
        .value_kind:     hidden_remainder_y
      - .offset:         54
        .size:           2
        .value_kind:     hidden_remainder_z
      - .offset:         72
        .size:           8
        .value_kind:     hidden_global_offset_x
      - .offset:         80
        .size:           8
        .value_kind:     hidden_global_offset_y
      - .offset:         88
        .size:           8
        .value_kind:     hidden_global_offset_z
      - .offset:         96
        .size:           2
        .value_kind:     hidden_grid_dims
      - .offset:         152
        .size:           4
        .value_kind:     hidden_dynamic_lds_size
    .group_segment_fixed_size: 0
    .kernarg_segment_align: 8
    .kernarg_segment_size: 288
    .language:       OpenCL C
    .language_version:
      - 2
      - 0
    .max_flat_workgroup_size: 256
    .name:           attn_fwd_pwg4x64
    .private_segment_fixed_size: 0
    .sgpr_count:     106
    .sgpr_spill_count: 0
    .symbol:         attn_fwd_pwg4x64.kd
    .uniform_work_group_size: 1
    .uses_dynamic_stack: false
    .vgpr_count:     508
    .vgpr_spill_count: 0
    .wavefront_size: 64
